# c36: c29 + MoE weight-conversion split rebalanced: IN1 filler converts 4 items per wave (was 6), class conversion 19 per wave (still 5 rounds)
# speedup vs baseline: 1.0015x; 1.0015x over previous
; #define DEEP_LOAD(I, v, idx) do { if ((idx) < hi) { moe_item(wg, wu, wd, wsb, (idx), I); xf8_load(I.W, I.N, I.k0, I.n0, lane, v); } } while (0)
; __device__ __forceinline__ void moe_item(const float* wg, const float* wu, const float* wd, unsigned char* wsb, int it, MoeItem& I) {
;     const int m = it / 1792, r = it - m * 1792, e = m / 3, kind = m - 3 * e;
;     if (kind < 2) { const int kb = r / 112, nb = r - kb * 112, n0 = 32 * nb;
;         I.W = (kind == 0 ? wg : wu) + (size_t)e * DM * FF; I.WT = wsb + WS_WMGU + (size_t)e * 2 * FF * DM; I.K = DM; I.N = FF; I.drow0 = 256 * (n0 >> 7) + (n0 & 127) + (kind == 1 ? 128 : 0); I.k0 = 64 * kb; I.n0 = n0; I.scale = 16.f; }
;     else { const int kb = r >> 5, nb = r & 31, n0 = 32 * nb;
;         I.W = wd + (size_t)e * FF * DM; I.WT = wsb + WS_WMD + (size_t)e * DM * FF; I.K = FF; I.N = DM; I.drow0 = n0; I.k0 = 64 * kb; I.n0 = n0; I.scale = 32.f; }
; }
; __device__ __forceinline__ void moe_deep_items(const float* wg, const float* wu, const float* wd, unsigned char* wsb, int lo, int hi, int first, int stride, LAS float* scr, int lane) {
;     ...
;     DEEP_LOAD(I0, v0, it); DEEP_LOAD(I1, v1, it + stride); DEEP_LOAD(I2, v2, it + 2 * stride); DEEP_LOAD(I3, v3, it + 3 * stride);
.LBB0_489:
	s_or_b64 exec, exec, s[14:15]
	s_and_b32 s0, s48, 0xff
	s_cmp_lg_u32 s0, 0
	s_waitcnt vmcnt(0) lgkmcnt(0)
	s_barrier
	s_cbranch_scc1 .LBB0_553
	s_add_i32 s32, s66, -2048
	s_add_i32 s6, s32, 0x1800
	s_cmp_lt_i32 s32, 0x9000
	s_cselect_b64 s[22:23], -1, 0
	s_cmp_gt_i32 s32, 0x8fff
	s_cbranch_scc1 .LBB0_494
	s_mul_hi_i32 s0, s6, 0x92492493
	s_add_i32 s0, s0, s6
	s_lshr_b32 s1, s0, 31
	s_ashr_i32 s0, s0, 10
	s_add_i32 s0, s0, s1
	s_mul_hi_i32 s1, s6, 0x30c30c31
	s_lshr_b32 s3, s1, 31
	s_ashr_i32 s4, s1, 10
	s_add_i32 s4, s4, s3
	s_mul_i32 s5, s0, 0xfffff900
	s_mul_i32 s3, s4, -3
	s_add_i32 s5, s5, s6
	s_add_i32 s3, s3, s0
	s_cmp_gt_i32 s3, 1
	s_mul_hi_i32 s7, s4, 0xe00000
	s_mul_i32 s19, s4, 0xe00000
	s_cbranch_scc0 .LBB0_498
	s_lshl_b32 s0, s32, 5
	s_and_b32 s38, s0, 0x3e0
	s_add_u32 s14, s60, s19
	s_addc_u32 s15, s61, s7
	s_mul_i32 s1, s4, 0x380000
	s_mul_hi_i32 s0, s4, 0x380000
	s_add_u32 s1, s34, s1
	s_addc_u32 s0, s35, s0
	s_add_u32 s8, s1, 0x7e00000
	s_addc_u32 s9, s0, 0
	s_lshl_b32 s0, s5, 1
	s_and_b32 s39, s0, 0xffffffc0
	s_cbranch_execz .LBB0_499
	s_mov_b32 s40, 0x42000000
	s_mov_b64 s[16:17], 0x400
	s_movk_i32 s41, 0xe00
	s_mov_b32 s18, s38
	s_branch .LBB0_500
.LBB0_494:
	v_mov_b32_e32 v29, 0
	v_mov_b32_e32 v28, v29
	v_mov_b32_e32 v27, v29
	v_mov_b32_e32 v26, v29
	v_mov_b32_e32 v33, v29
	v_mov_b32_e32 v32, v29
	v_mov_b32_e32 v31, v29
	v_mov_b32_e32 v30, v29
	v_mov_b32_e32 v21, v29
	v_mov_b32_e32 v20, v29
	v_mov_b32_e32 v19, v29
	v_mov_b32_e32 v18, v29
	v_mov_b32_e32 v25, v29
	v_mov_b32_e32 v24, v29
	v_mov_b32_e32 v23, v29
	v_mov_b32_e32 v22, v29
	v_mov_b32_e32 v13, v29
	v_mov_b32_e32 v12, v29
	v_mov_b32_e32 v11, v29
	v_mov_b32_e32 v10, v29
	v_mov_b32_e32 v17, v29
	v_mov_b32_e32 v16, v29
	v_mov_b32_e32 v15, v29
	v_mov_b32_e32 v14, v29
	v_mov_b32_e32 v5, v29
	v_mov_b32_e32 v4, v29
	v_mov_b32_e32 v3, v29
	v_mov_b32_e32 v2, v29
	v_mov_b32_e32 v9, v29
	v_mov_b32_e32 v8, v29
	v_mov_b32_e32 v7, v29
	v_mov_b32_e32 v6, v29
	s_cmp_gt_i32 s32, 0x87ff
	s_cbranch_scc0 .LBB0_501
.LBB0_495:
	s_cmpk_gt_i32 s32, 0x7fff
	s_cbranch_scc0 .LBB0_507
.LBB0_496:
	s_cmpk_gt_i32 s32, 0x77ff
	s_cbranch_scc0 .LBB0_513

; #define GAS __attribute__((address_space(1)))
; __device__ __forceinline__ void xf8_load(const float* W, int N, int k0, int n0, int lane, f32x4 (&v)[8]) {
; #pragma unroll
;     for (int i = 0; i < 8; ++i) v[i] = __builtin_nontemporal_load((const GAS f32x4*)(W + (size_t)(k0 + 8 * i + (lane >> 3)) * N + n0 + 4 * (lane & 7)));
; }
; __device__ __forceinline__ void moe_item(const float* wg, const float* wu, const float* wd, unsigned char* wsb, int it, MoeItem& I) {
;     const int m = it / 1792, r = it - m * 1792, e = m / 3, kind = m - 3 * e;
;     if (kind < 2) { const int kb = r / 112, nb = r - kb * 112, n0 = 32 * nb;
;         I.W = (kind == 0 ? wg : wu) + (size_t)e * DM * FF; I.WT = wsb + WS_WMGU + (size_t)e * 2 * FF * DM; I.K = DM; I.N = FF; I.drow0 = 256 * (n0 >> 7) + (n0 & 127) + (kind == 1 ? 128 : 0); I.k0 = 64 * kb; I.n0 = n0; I.scale = 16.f; }
;     else { const int kb = r >> 5, nb = r & 31, n0 = 32 * nb;
;         I.W = wd + (size_t)e * FF * DM; I.WT = wsb + WS_WMD + (size_t)e * DM * FF; I.K = FF; I.N = DM; I.drow0 = n0; I.k0 = 64 * kb; I.n0 = n0; I.scale = 32.f; }
; }
.LBB0_500:
	s_ashr_i32 s19, s18, 31
	v_lshrrev_b32_e32 v2, 3, v162
	s_lshl_b64 s[4:5], s[18:19], 2
	v_or_b32_e32 v30, s39, v2
	s_add_u32 s4, s14, s4
	v_lshlrev_b32_e32 v2, 4, v0
	s_addc_u32 s5, s15, s5
	v_and_b32_e32 v2, 0x70, v2
	v_mov_b32_e32 v3, 0
	v_lshl_add_u64 v[26:27], s[4:5], 0, v[2:3]
	v_mad_i64_i32 v[2:3], s[4:5], s16, v30, 0
	v_or_b32_e32 v4, 8, v30
	v_or_b32_e32 v10, 16, v30
	v_or_b32_e32 v12, 24, v30
	v_or_b32_e32 v18, 32, v30
	v_or_b32_e32 v20, 40, v30
	v_or_b32_e32 v28, 48, v30
	v_or_b32_e32 v30, 56, v30
	v_mad_i64_i32 v[4:5], s[4:5], s16, v4, 0
	v_mad_i64_i32 v[10:11], s[4:5], s16, v10, 0
	v_mad_i64_i32 v[12:13], s[4:5], s16, v12, 0
	v_mad_i64_i32 v[18:19], s[4:5], s16, v18, 0
	v_mad_i64_i32 v[20:21], s[4:5], s16, v20, 0
	v_mad_i64_i32 v[28:29], s[4:5], s16, v28, 0
	v_mad_i64_i32 v[30:31], s[4:5], s16, v30, 0
	v_lshl_add_u64 v[2:3], v[2:3], 2, v[26:27]
	v_lshl_add_u64 v[4:5], v[4:5], 2, v[26:27]
	v_lshl_add_u64 v[10:11], v[10:11], 2, v[26:27]
	v_lshl_add_u64 v[12:13], v[12:13], 2, v[26:27]
	v_lshl_add_u64 v[18:19], v[18:19], 2, v[26:27]
	v_lshl_add_u64 v[20:21], v[20:21], 2, v[26:27]
	v_lshl_add_u64 v[28:29], v[28:29], 2, v[26:27]
	v_lshl_add_u64 v[26:27], v[30:31], 2, v[26:27]
	global_load_dwordx4 v[6:9], v[2:3], off nt
	s_nop 0
	global_load_dwordx4 v[2:5], v[4:5], off nt
	s_nop 0
	global_load_dwordx4 v[14:17], v[10:11], off nt
	s_nop 0
	global_load_dwordx4 v[10:13], v[12:13], off nt
	s_nop 0
	global_load_dwordx4 v[22:25], v[18:19], off nt
	s_nop 0
	global_load_dwordx4 v[18:21], v[20:21], off nt
	s_nop 0
	global_load_dwordx4 v[30:33], v[28:29], off nt
	s_nop 0
	global_load_dwordx4 v[26:29], v[26:27], off nt
	s_cmp_gt_i32 s32, 0x87ff
	s_cbranch_scc1 .LBB0_495
.LBB0_501:
	s_add_i32 s0, s32, 0x2000
	s_mul_hi_i32 s1, s0, 0x92492493
	s_add_i32 s1, s1, s0
	s_lshr_b32 s3, s1, 31
	s_ashr_i32 s1, s1, 10
	s_add_i32 s1, s1, s3
	s_mul_i32 s5, s1, 0xfffff900
	s_add_i32 s5, s5, s0
	s_mul_hi_i32 s0, s0, 0x30c30c31
	s_lshr_b32 s3, s0, 31
	s_ashr_i32 s4, s0, 10
	s_add_i32 s4, s4, s3
	s_mul_i32 s3, s4, -3
	s_add_i32 s3, s3, s1
	s_cmp_gt_i32 s3, 1
	s_mul_hi_i32 s7, s4, 0xe00000
	s_mul_i32 s25, s4, 0xe00000
	s_cbranch_scc0 .LBB0_504
	s_lshl_b32 s0, s32, 5
	s_and_b32 s42, s0, 0x3e0
	s_add_u32 s16, s60, s25
	s_addc_u32 s17, s61, s7
	s_mul_i32 s1, s4, 0x380000
	s_mul_hi_i32 s0, s4, 0x380000
	s_add_u32 s1, s34, s1
	s_addc_u32 s0, s35, s0
	s_add_u32 s14, s1, 0x7e00000
	s_addc_u32 s15, s0, 0
	s_lshl_b32 s0, s5, 1
	s_and_b32 s43, s0, 0xffffffc0
	s_cbranch_execz .LBB0_505
	s_mov_b32 s44, 0x42000000
	s_mov_b64 s[18:19], 0x400
	s_movk_i32 s45, 0xe00
	s_mov_b32 s24, s42
	s_branch .LBB0_506

; #define GAS __attribute__((address_space(1)))
; __device__ __forceinline__ void xf8_load(const float* W, int N, int k0, int n0, int lane, f32x4 (&v)[8]) {
; #pragma unroll
;     for (int i = 0; i < 8; ++i) v[i] = __builtin_nontemporal_load((const GAS f32x4*)(W + (size_t)(k0 + 8 * i + (lane >> 3)) * N + n0 + 4 * (lane & 7)));
; }
; __device__ __forceinline__ void moe_item(const float* wg, const float* wu, const float* wd, unsigned char* wsb, int it, MoeItem& I) {
;     const int m = it / 1792, r = it - m * 1792, e = m / 3, kind = m - 3 * e;
;     if (kind < 2) { const int kb = r / 112, nb = r - kb * 112, n0 = 32 * nb;
;         I.W = (kind == 0 ? wg : wu) + (size_t)e * DM * FF; I.WT = wsb + WS_WMGU + (size_t)e * 2 * FF * DM; I.K = DM; I.N = FF; I.drow0 = 256 * (n0 >> 7) + (n0 & 127) + (kind == 1 ? 128 : 0); I.k0 = 64 * kb; I.n0 = n0; I.scale = 16.f; }
;     else { const int kb = r >> 5, nb = r & 31, n0 = 32 * nb;
;         I.W = wd + (size_t)e * FF * DM; I.WT = wsb + WS_WMD + (size_t)e * DM * FF; I.K = FF; I.N = DM; I.drow0 = n0; I.k0 = 64 * kb; I.n0 = n0; I.scale = 32.f; }
; }
.LBB0_506:
	s_ashr_i32 s25, s24, 31
	v_lshrrev_b32_e32 v34, 3, v162
	s_lshl_b64 s[4:5], s[24:25], 2
	v_or_b32_e32 v62, s43, v34
	s_add_u32 s4, s16, s4
	v_lshlrev_b32_e32 v34, 4, v0
	s_addc_u32 s5, s17, s5
	v_and_b32_e32 v34, 0x70, v34
	v_mov_b32_e32 v35, 0
	v_lshl_add_u64 v[58:59], s[4:5], 0, v[34:35]
	v_mad_i64_i32 v[34:35], s[4:5], s18, v62, 0
	v_or_b32_e32 v36, 8, v62
	v_or_b32_e32 v42, 16, v62
	v_or_b32_e32 v44, 24, v62
	v_or_b32_e32 v50, 32, v62
	v_or_b32_e32 v52, 40, v62
	v_or_b32_e32 v60, 48, v62
	v_or_b32_e32 v62, 56, v62
	v_mad_i64_i32 v[36:37], s[4:5], s18, v36, 0
	v_mad_i64_i32 v[42:43], s[4:5], s18, v42, 0
	v_mad_i64_i32 v[44:45], s[4:5], s18, v44, 0
	v_mad_i64_i32 v[50:51], s[4:5], s18, v50, 0
	v_mad_i64_i32 v[52:53], s[4:5], s18, v52, 0
	v_mad_i64_i32 v[60:61], s[4:5], s18, v60, 0
	v_mad_i64_i32 v[62:63], s[4:5], s18, v62, 0
	v_lshl_add_u64 v[34:35], v[34:35], 2, v[58:59]
	v_lshl_add_u64 v[38:39], v[36:37], 2, v[58:59]
	v_lshl_add_u64 v[42:43], v[42:43], 2, v[58:59]
	v_lshl_add_u64 v[46:47], v[44:45], 2, v[58:59]
	v_lshl_add_u64 v[50:51], v[50:51], 2, v[58:59]
	v_lshl_add_u64 v[54:55], v[52:53], 2, v[58:59]
	v_lshl_add_u64 v[60:61], v[60:61], 2, v[58:59]
	v_lshl_add_u64 v[62:63], v[62:63], 2, v[58:59]
	global_load_dwordx4 v[34:37], v[34:35], off nt
	s_nop 0
	global_load_dwordx4 v[38:41], v[38:39], off nt
	s_nop 0
	global_load_dwordx4 v[42:45], v[42:43], off nt
	s_nop 0
	global_load_dwordx4 v[46:49], v[46:47], off nt
	s_nop 0
	global_load_dwordx4 v[50:53], v[50:51], off nt
	s_nop 0
	global_load_dwordx4 v[54:57], v[54:55], off nt
	s_nop 0
	global_load_dwordx4 v[58:61], v[60:61], off nt
	s_nop 0
	global_load_dwordx4 v[62:65], v[62:63], off nt
	s_cmpk_gt_i32 s32, 0x7fff
	s_cbranch_scc1 .LBB0_496
.LBB0_507:
	s_add_i32 s0, s32, 0x2800
	s_mul_hi_i32 s1, s0, 0x92492493
	s_add_i32 s1, s1, s0
	s_lshr_b32 s3, s1, 31
	s_ashr_i32 s1, s1, 10
	s_add_i32 s1, s1, s3
	s_mul_i32 s5, s1, 0xfffff900
	s_add_i32 s5, s5, s0
	s_mul_hi_i32 s0, s0, 0x30c30c31
	s_lshr_b32 s3, s0, 31
	s_ashr_i32 s4, s0, 10
	s_add_i32 s4, s4, s3
	s_mul_i32 s3, s4, -3
	s_add_i32 s3, s3, s1
	s_cmp_gt_i32 s3, 1
	s_mul_hi_i32 s7, s4, 0xe00000
	s_mul_i32 s31, s4, 0xe00000
	s_cbranch_scc0 .LBB0_510
	s_lshl_b32 s0, s32, 5
	s_and_b32 s46, s0, 0x3e0
	s_add_u32 s18, s60, s31
	s_addc_u32 s19, s61, s7
	s_mul_i32 s1, s4, 0x380000
	s_mul_hi_i32 s0, s4, 0x380000
	s_add_u32 s1, s34, s1
	s_addc_u32 s0, s35, s0
	s_add_u32 s16, s1, 0x7e00000
	s_addc_u32 s17, s0, 0
	s_lshl_b32 s0, s5, 1
	s_and_b32 s47, s0, 0xffffffc0
	s_cbranch_execz .LBB0_511
	s_mov_b32 s49, 0x42000000
	s_mov_b64 s[24:25], 0x400
	s_movk_i32 s50, 0xe00
	s_mov_b32 s30, s46
	s_branch .LBB0_512

; #define GAS __attribute__((address_space(1)))
; __device__ __forceinline__ void xf8_load(const float* W, int N, int k0, int n0, int lane, f32x4 (&v)[8]) {
; #pragma unroll
;     for (int i = 0; i < 8; ++i) v[i] = __builtin_nontemporal_load((const GAS f32x4*)(W + (size_t)(k0 + 8 * i + (lane >> 3)) * N + n0 + 4 * (lane & 7)));
; }
; __device__ __forceinline__ void moe_item(const float* wg, const float* wu, const float* wd, unsigned char* wsb, int it, MoeItem& I) {
;     const int m = it / 1792, r = it - m * 1792, e = m / 3, kind = m - 3 * e;
;     if (kind < 2) { const int kb = r / 112, nb = r - kb * 112, n0 = 32 * nb;
;         I.W = (kind == 0 ? wg : wu) + (size_t)e * DM * FF; I.WT = wsb + WS_WMGU + (size_t)e * 2 * FF * DM; I.K = DM; I.N = FF; I.drow0 = 256 * (n0 >> 7) + (n0 & 127) + (kind == 1 ? 128 : 0); I.k0 = 64 * kb; I.n0 = n0; I.scale = 16.f; }
;     else { const int kb = r >> 5, nb = r & 31, n0 = 32 * nb;
;         I.W = wd + (size_t)e * FF * DM; I.WT = wsb + WS_WMD + (size_t)e * DM * FF; I.K = FF; I.N = DM; I.drow0 = n0; I.k0 = 64 * kb; I.n0 = n0; I.scale = 32.f; }
; }
.LBB0_512:
	s_ashr_i32 s31, s30, 31
	v_lshrrev_b32_e32 v66, 3, v162
	s_lshl_b64 s[4:5], s[30:31], 2
	v_or_b32_e32 v94, s47, v66
	s_add_u32 s4, s18, s4
	v_lshlrev_b32_e32 v66, 4, v0
	s_addc_u32 s5, s19, s5
	v_and_b32_e32 v66, 0x70, v66
	v_mov_b32_e32 v67, 0
	v_lshl_add_u64 v[90:91], s[4:5], 0, v[66:67]
	v_mad_i64_i32 v[66:67], s[4:5], s24, v94, 0
	v_or_b32_e32 v68, 8, v94
	v_or_b32_e32 v74, 16, v94
	v_or_b32_e32 v76, 24, v94
	v_or_b32_e32 v82, 32, v94
	v_or_b32_e32 v84, 40, v94
	v_or_b32_e32 v92, 48, v94
	v_or_b32_e32 v94, 56, v94
	v_mad_i64_i32 v[68:69], s[4:5], s24, v68, 0
	v_mad_i64_i32 v[74:75], s[4:5], s24, v74, 0
	v_mad_i64_i32 v[76:77], s[4:5], s24, v76, 0
	v_mad_i64_i32 v[82:83], s[4:5], s24, v82, 0
	v_mad_i64_i32 v[84:85], s[4:5], s24, v84, 0
	v_mad_i64_i32 v[92:93], s[4:5], s24, v92, 0
	v_mad_i64_i32 v[94:95], s[4:5], s24, v94, 0
	v_lshl_add_u64 v[66:67], v[66:67], 2, v[90:91]
	v_lshl_add_u64 v[70:71], v[68:69], 2, v[90:91]
	v_lshl_add_u64 v[74:75], v[74:75], 2, v[90:91]
	v_lshl_add_u64 v[78:79], v[76:77], 2, v[90:91]
	v_lshl_add_u64 v[82:83], v[82:83], 2, v[90:91]
	v_lshl_add_u64 v[86:87], v[84:85], 2, v[90:91]
	v_lshl_add_u64 v[92:93], v[92:93], 2, v[90:91]
	v_lshl_add_u64 v[94:95], v[94:95], 2, v[90:91]
	global_load_dwordx4 v[66:69], v[66:67], off nt
	s_nop 0
	global_load_dwordx4 v[70:73], v[70:71], off nt
	s_nop 0
	global_load_dwordx4 v[74:77], v[74:75], off nt
	s_nop 0
	global_load_dwordx4 v[78:81], v[78:79], off nt
	s_nop 0
	global_load_dwordx4 v[82:85], v[82:83], off nt
	s_nop 0
	global_load_dwordx4 v[86:89], v[86:87], off nt
	s_nop 0
	global_load_dwordx4 v[90:93], v[92:93], off nt
	s_nop 0
	global_load_dwordx4 v[94:97], v[94:95], off nt
	s_cmpk_gt_i32 s32, 0x77ff
	s_cbranch_scc1 .LBB0_497
.LBB0_513:
	s_add_i32 s0, s32, 0x3000
	s_mul_hi_i32 s1, s0, 0x92492493
	s_add_i32 s1, s1, s0
	s_lshr_b32 s3, s1, 31
	s_ashr_i32 s1, s1, 10
	s_add_i32 s1, s1, s3
	s_mul_i32 s5, s1, 0xfffff900
	s_add_i32 s5, s5, s0
	s_mul_hi_i32 s0, s0, 0x30c30c31
	s_lshr_b32 s3, s0, 31
	s_ashr_i32 s4, s0, 10
	s_add_i32 s4, s4, s3
	s_mul_i32 s3, s4, -3
	s_add_i32 s3, s3, s1
	s_cmp_gt_i32 s3, 1
	s_mul_hi_i32 s7, s4, 0xe00000
	s_mul_i32 s33, s4, 0xe00000
	s_cbranch_scc0 .LBB0_516
	s_lshl_b32 s0, s32, 5
	s_and_b32 s51, s0, 0x3e0
	s_add_u32 s24, s60, s33
	s_addc_u32 s25, s61, s7
	s_mul_i32 s1, s4, 0x380000
	s_mul_hi_i32 s0, s4, 0x380000
	s_add_u32 s1, s34, s1
	s_addc_u32 s0, s35, s0
	s_add_u32 s18, s1, 0x7e00000
	s_addc_u32 s19, s0, 0
	s_lshl_b32 s0, s5, 1
	s_and_b32 s52, s0, 0xffffffc0
	s_cbranch_execz .LBB0_517
	s_mov_b32 s53, 0x42000000
	s_mov_b64 s[30:31], 0x400
	s_movk_i32 s70, 0xe00
	s_mov_b32 s36, s51
	s_branch .LBB0_518

; __device__ __forceinline__ unsigned pk4_fp8(float a, float b, float c, float d) { int w = 0; w = __builtin_amdgcn_cvt_pk_fp8_f32(a, b, w, false); w = __builtin_amdgcn_cvt_pk_fp8_f32(c, d, w, true); return (unsigned)w; }
; #define GAS __attribute__((address_space(1)))
; #define LAS __attribute__((address_space(3)))
; #define LDS_WAIT() asm volatile("s_waitcnt lgkmcnt(0)" ::: "memory")
; #define DEEP_LOAD(I, v, idx) do { if ((idx) < hi) { moe_item(wg, wu, wd, wsb, (idx), I); xf8_load(I.W, I.N, I.k0, I.n0, lane, v); } } while (0)
; #define DEEP_STEP(I, v, idx) do { if ((idx) < hi) { xf8_proc(v, I.K, I.WT, I.drow0, I.k0, I.scale, scr, lane); DEEP_LOAD(I, v, (idx) + 4 * stride); } } while (0)
; __device__ __forceinline__ void xf8_proc(const f32x4 (&v)[8], int K, unsigned char* WT, int drow0, int k0, float scale, LAS float* scr, int lane) {
; #pragma unroll
;     for (int i = 0; i < 8; ++i) { LAS float* d_ = scr + (8 * i + (lane >> 3)) * 33 + 4 * (lane & 7); d_[0] = v[i].x; d_[1] = v[i].y; d_[2] = v[i].z; d_[3] = v[i].w; }
;     LDS_WAIT(); asm volatile("" ::: "memory");
;     const int c = lane & 7;
; #pragma unroll
;     for (int j = 0; j < 4; ++j) { const int n = (lane >> 3) + 8 * j; const LAS float* s = scr + (8 * c) * 33 + n;
;         pg8::u32x2 o; o.x = pg8::pk4_fp8(s[0 * 33] * scale, s[1 * 33] * scale, s[2 * 33] * scale, s[3 * 33] * scale); o.y = pg8::pk4_fp8(s[4 * 33] * scale, s[5 * 33] * scale, s[6 * 33] * scale, s[7 * 33] * scale);
;         __builtin_nontemporal_store(o, (GAS pg8::u32x2*)(WT + (size_t)(drow0 + n) * K + k0 + 8 * c)); }
;     LDS_WAIT(); asm volatile("" ::: "memory");
; }
; __device__ __forceinline__ void moe_deep_items(const float* wg, const float* wu, const float* wd, unsigned char* wsb, int lo, int hi, int first, int stride, LAS float* scr, int lane) {
;     ...
;     DEEP_LOAD(I0, v0, it); DEEP_LOAD(I1, v1, it + stride); DEEP_LOAD(I2, v2, it + 2 * stride); DEEP_LOAD(I3, v3, it + 3 * stride);
;     for (; it < hi; it += 4 * stride) { DEEP_STEP(I0, v0, it); DEEP_STEP(I1, v1, it + stride); DEEP_STEP(I2, v2, it + 2 * stride); DEEP_STEP(I3, v3, it + 3 * stride); }
.LBB0_519:
	s_lshl_b32 s0, s82, 14
	s_add_i32 s0, s0, 0
	v_lshlrev_b32_e32 v130, 2, v0
	v_lshlrev_b32_e32 v132, 3, v0
	s_add_u32 s36, s34, 0x7e00000
	v_lshrrev_b32_e32 v131, 3, v162
	v_and_b32_e32 v130, 28, v130
	v_and_b32_e32 v132, 56, v132
	s_addc_u32 s37, s35, 0
	v_lshl_add_u32 v134, v130, 2, s0
	v_mul_u32_u24_e32 v140, 0x84, v131
	v_mul_u32_u24_e32 v139, 0x84, v132
	v_lshlrev_b32_e32 v141, 2, v131
	s_add_u32 s71, s34, 0x4600000
	v_mov_b32_e32 v135, 0
	v_add3_u32 v139, s0, v139, v141
	s_addc_u32 s72, s35, 0
	s_lshl_b32 s0, s2, 4
	s_lshl_b32 s1, s82, 1
	v_add_u32_e32 v140, v134, v140
	v_or_b32_e32 v136, 8, v131
	v_or_b32_e32 v137, 16, v131
	v_or_b32_e32 v138, 24, v131
	v_mov_b32_e32 v133, v135
	s_add_i32 s73, s32, 0x5000
	s_add_i32 s74, s0, s1
	s_addk_i32 s74, -4096
	s_lshl_b32 s75, s6, 5
	v_add_u32_e32 v141, 0x420, v140
	v_add_u32_e32 v142, 0x428, v140
	v_add_u32_e32 v143, 0x840, v140
	v_add_u32_e32 v144, 0x848, v140
	v_add_u32_e32 v145, 0xc60, v140
	v_add_u32_e32 v146, 0xc68, v140
	v_add_u32_e32 v147, 0x1080, v140
	v_add_u32_e32 v148, 0x1088, v140
	v_add_u32_e32 v149, 0x14a0, v140
	v_add_u32_e32 v150, 0x14a8, v140
	v_add_u32_e32 v151, 0x18c0, v140
	v_add_u32_e32 v152, 0x18c8, v140
	v_add_u32_e32 v153, 0x1ce0, v140
	v_add_u32_e32 v154, 0x1ce8, v140
	s_branch .LBB0_523

; #define LAS __attribute__((address_space(3)))
; __device__ __forceinline__ void moe_item(const float* wg, const float* wu, const float* wd, unsigned char* wsb, int it, MoeItem& I) {
;     const int m = it / 1792, r = it - m * 1792, e = m / 3, kind = m - 3 * e;
;     if (kind < 2) { const int kb = r / 112, nb = r - kb * 112, n0 = 32 * nb;
;         I.W = (kind == 0 ? wg : wu) + (size_t)e * DM * FF; I.WT = wsb + WS_WMGU + (size_t)e * 2 * FF * DM; I.K = DM; I.N = FF; I.drow0 = 256 * (n0 >> 7) + (n0 & 127) + (kind == 1 ? 128 : 0); I.k0 = 64 * kb; I.n0 = n0; I.scale = 16.f; }
;     else { const int kb = r >> 5, nb = r & 31, n0 = 32 * nb;
;         I.W = wd + (size_t)e * FF * DM; I.WT = wsb + WS_WMD + (size_t)e * DM * FF; I.K = FF; I.N = DM; I.drow0 = n0; I.k0 = 64 * kb; I.n0 = n0; I.scale = 32.f; }
; }
; __global__ void __launch_bounds__(NTHREADS, 2) fwd(Args args) {
;     ...
;     if (IN(PH_D0)) {
;         pg8::Gemm g{HID0, (const bf16*)(ws + WS_WD0), SEQ, DM, FF, 0}; pg8::StaticOrder S; S.init(SEQ, DM, GRID, F.bid);
;         pg8::EpiResF32 E{nullptr, HN, nullptr, DM, HN, SS1, MISC_OFF + 1024, HN8A};
;         LAS float* cscr = (LAS float*)(F.lds + RING_OFF + F.wave * 16384);
;         if (conv_cls == 1) { moe_deep_items(args.in[18], args.in[19], args.in[20], ws, FILL1 + FILL2, MOE_ITEMS, gw, NGW, cscr, F.lane); __syncthreads(); }
.LBB0_590:
	s_cmp_lt_i32 s64, 6
	s_cselect_b64 s[4:5], -1, 0
	s_and_b64 s[18:19], s[4:5], s[8:9]
	s_andn2_b64 vcc, exec, s[18:19]
	s_cbranch_vccnz .LBB0_767
	s_lshl_b32 s0, s82, 14
	s_add_i32 s72, s0, 0
	s_and_b32 s73, s48, 0xff
	s_cmp_lg_u32 s73, 1
	s_cbranch_scc1 .LBB0_655
	s_add_i32 s32, s66, -2048
	s_add_i32 s6, s32, 0x1800
	s_cmp_lt_i32 s32, 0x9000
	s_cselect_b64 s[16:17], -1, 0
	s_cmp_gt_i32 s32, 0x8fff
	s_cbranch_scc1 .LBB0_596
	s_mul_hi_i32 s0, s6, 0x92492493
	s_add_i32 s0, s0, s6
	s_lshr_b32 s1, s0, 31
	s_ashr_i32 s0, s0, 10
	s_add_i32 s0, s0, s1
	s_mul_hi_i32 s1, s6, 0x30c30c31
	s_lshr_b32 s3, s1, 31
	s_ashr_i32 s4, s1, 10
	s_add_i32 s4, s4, s3
	s_mul_i32 s5, s0, 0xfffff900
	s_mul_i32 s3, s4, -3
	s_add_i32 s5, s5, s6
	s_add_i32 s3, s3, s0
	s_cmp_gt_i32 s3, 1
	s_mul_hi_i32 s7, s4, 0xe00000
	s_mul_i32 s15, s4, 0xe00000
	s_cbranch_scc0 .LBB0_600
	s_lshl_b32 s0, s32, 5
	s_and_b32 s36, s0, 0x3e0
	s_add_u32 s10, s60, s15
	s_addc_u32 s11, s61, s7
	s_mul_i32 s1, s4, 0x380000
	s_mul_hi_i32 s0, s4, 0x380000
	s_add_u32 s1, s34, s1
	s_addc_u32 s0, s35, s0
	s_add_u32 s8, s1, 0x7e00000
	s_addc_u32 s9, s0, 0
	s_lshl_b32 s0, s5, 1
	s_and_b32 s37, s0, 0xffffffc0
	s_cbranch_execz .LBB0_601
	s_mov_b32 s38, 0x42000000
	s_mov_b64 s[12:13], 0x400
	s_movk_i32 s39, 0xe00
	s_mov_b32 s14, s36
	s_branch .LBB0_602
.LBB0_596:
	s_waitcnt vmcnt(0)
	v_mov_b32_e32 v29, 0
	v_mov_b32_e32 v28, v29
	v_mov_b32_e32 v27, v29
	v_mov_b32_e32 v26, v29
	v_mov_b32_e32 v33, v29
	v_mov_b32_e32 v32, v29
	v_mov_b32_e32 v31, v29
	v_mov_b32_e32 v30, v29
	v_mov_b32_e32 v21, v29
	v_mov_b32_e32 v20, v29
	v_mov_b32_e32 v19, v29
	v_mov_b32_e32 v18, v29
	v_mov_b32_e32 v25, v29
	v_mov_b32_e32 v24, v29
	v_mov_b32_e32 v23, v29
	v_mov_b32_e32 v22, v29
	v_mov_b32_e32 v13, v29
	v_mov_b32_e32 v12, v29
	v_mov_b32_e32 v11, v29
	v_mov_b32_e32 v10, v29
	v_mov_b32_e32 v17, v29
	v_mov_b32_e32 v16, v29
	v_mov_b32_e32 v15, v29
	v_mov_b32_e32 v14, v29
	v_mov_b32_e32 v5, v29
	v_mov_b32_e32 v4, v29
	v_mov_b32_e32 v3, v29
	v_mov_b32_e32 v2, v29
	v_mov_b32_e32 v9, v29
	v_mov_b32_e32 v8, v29
	v_mov_b32_e32 v7, v29
	v_mov_b32_e32 v6, v29
	s_cmp_gt_i32 s32, 0x87ff
	s_cbranch_scc0 .LBB0_603

; #define GAS __attribute__((address_space(1)))
; __device__ __forceinline__ void xf8_load(const float* W, int N, int k0, int n0, int lane, f32x4 (&v)[8]) {
; #pragma unroll
;     for (int i = 0; i < 8; ++i) v[i] = __builtin_nontemporal_load((const GAS f32x4*)(W + (size_t)(k0 + 8 * i + (lane >> 3)) * N + n0 + 4 * (lane & 7)));
; }
; __device__ __forceinline__ void moe_item(const float* wg, const float* wu, const float* wd, unsigned char* wsb, int it, MoeItem& I) {
;     const int m = it / 1792, r = it - m * 1792, e = m / 3, kind = m - 3 * e;
;     if (kind < 2) { const int kb = r / 112, nb = r - kb * 112, n0 = 32 * nb;
;         I.W = (kind == 0 ? wg : wu) + (size_t)e * DM * FF; I.WT = wsb + WS_WMGU + (size_t)e * 2 * FF * DM; I.K = DM; I.N = FF; I.drow0 = 256 * (n0 >> 7) + (n0 & 127) + (kind == 1 ? 128 : 0); I.k0 = 64 * kb; I.n0 = n0; I.scale = 16.f; }
;     else { const int kb = r >> 5, nb = r & 31, n0 = 32 * nb;
;         I.W = wd + (size_t)e * FF * DM; I.WT = wsb + WS_WMD + (size_t)e * DM * FF; I.K = FF; I.N = DM; I.drow0 = n0; I.k0 = 64 * kb; I.n0 = n0; I.scale = 32.f; }
; }
.LBB0_602:
	s_ashr_i32 s15, s14, 31
	s_waitcnt vmcnt(0)
	v_lshrrev_b32_e32 v2, 3, v162
	s_lshl_b64 s[4:5], s[14:15], 2
	v_or_b32_e32 v30, s37, v2
	s_add_u32 s4, s10, s4
	v_lshlrev_b32_e32 v2, 4, v0
	s_addc_u32 s5, s11, s5
	v_and_b32_e32 v2, 0x70, v2
	v_mov_b32_e32 v3, 0
	v_lshl_add_u64 v[26:27], s[4:5], 0, v[2:3]
	v_mad_i64_i32 v[2:3], s[4:5], s12, v30, 0
	v_or_b32_e32 v4, 8, v30
	v_or_b32_e32 v10, 16, v30
	v_or_b32_e32 v12, 24, v30
	v_or_b32_e32 v18, 32, v30
	v_or_b32_e32 v20, 40, v30
	v_or_b32_e32 v28, 48, v30
	v_or_b32_e32 v30, 56, v30
	v_mad_i64_i32 v[4:5], s[4:5], s12, v4, 0
	v_mad_i64_i32 v[10:11], s[4:5], s12, v10, 0
	v_mad_i64_i32 v[12:13], s[4:5], s12, v12, 0
	v_mad_i64_i32 v[18:19], s[4:5], s12, v18, 0
	v_mad_i64_i32 v[20:21], s[4:5], s12, v20, 0
	v_mad_i64_i32 v[28:29], s[4:5], s12, v28, 0
	v_mad_i64_i32 v[30:31], s[4:5], s12, v30, 0
	v_lshl_add_u64 v[2:3], v[2:3], 2, v[26:27]
	v_lshl_add_u64 v[4:5], v[4:5], 2, v[26:27]
	v_lshl_add_u64 v[10:11], v[10:11], 2, v[26:27]
	v_lshl_add_u64 v[12:13], v[12:13], 2, v[26:27]
	v_lshl_add_u64 v[18:19], v[18:19], 2, v[26:27]
	v_lshl_add_u64 v[20:21], v[20:21], 2, v[26:27]
	v_lshl_add_u64 v[28:29], v[28:29], 2, v[26:27]
	v_lshl_add_u64 v[26:27], v[30:31], 2, v[26:27]
	global_load_dwordx4 v[6:9], v[2:3], off nt
	s_nop 0
	global_load_dwordx4 v[2:5], v[4:5], off nt
	s_nop 0
	global_load_dwordx4 v[14:17], v[10:11], off nt
	s_nop 0
	global_load_dwordx4 v[10:13], v[12:13], off nt
	s_nop 0
	global_load_dwordx4 v[22:25], v[18:19], off nt
	s_nop 0
	global_load_dwordx4 v[18:21], v[20:21], off nt
	s_nop 0
	global_load_dwordx4 v[30:33], v[28:29], off nt
	s_nop 0
	global_load_dwordx4 v[26:29], v[26:27], off nt
	s_cmp_gt_i32 s32, 0x87ff
	s_cbranch_scc1 .LBB0_597
.LBB0_603:
	s_add_i32 s0, s32, 0x2000
	s_mul_hi_i32 s1, s0, 0x92492493
	s_add_i32 s1, s1, s0
	s_lshr_b32 s3, s1, 31
	s_ashr_i32 s1, s1, 10
	s_add_i32 s1, s1, s3
	s_mul_i32 s5, s1, 0xfffff900
	s_add_i32 s5, s5, s0
	s_mul_hi_i32 s0, s0, 0x30c30c31
	s_lshr_b32 s3, s0, 31
	s_ashr_i32 s4, s0, 10
	s_add_i32 s4, s4, s3
	s_mul_i32 s3, s4, -3
	s_add_i32 s3, s3, s1
	s_cmp_gt_i32 s3, 1
	s_mul_hi_i32 s7, s4, 0xe00000
	s_mul_i32 s23, s4, 0xe00000
	s_cbranch_scc0 .LBB0_606
	s_lshl_b32 s0, s32, 5
	s_and_b32 s40, s0, 0x3e0
	s_add_u32 s12, s60, s23
	s_addc_u32 s13, s61, s7
	s_mul_i32 s1, s4, 0x380000
	s_mul_hi_i32 s0, s4, 0x380000
	s_add_u32 s1, s34, s1
	s_addc_u32 s0, s35, s0
	s_add_u32 s10, s1, 0x7e00000
	s_addc_u32 s11, s0, 0
	s_lshl_b32 s0, s5, 1
	s_and_b32 s41, s0, 0xffffffc0
	s_cbranch_execz .LBB0_607
	s_mov_b32 s42, 0x42000000
	s_mov_b64 s[14:15], 0x400
	s_movk_i32 s43, 0xe00
	s_mov_b32 s22, s40
	s_branch .LBB0_608

; #define GAS __attribute__((address_space(1)))
; __device__ __forceinline__ void xf8_load(const float* W, int N, int k0, int n0, int lane, f32x4 (&v)[8]) {
; #pragma unroll
;     for (int i = 0; i < 8; ++i) v[i] = __builtin_nontemporal_load((const GAS f32x4*)(W + (size_t)(k0 + 8 * i + (lane >> 3)) * N + n0 + 4 * (lane & 7)));
; }
; __device__ __forceinline__ void moe_item(const float* wg, const float* wu, const float* wd, unsigned char* wsb, int it, MoeItem& I) {
;     const int m = it / 1792, r = it - m * 1792, e = m / 3, kind = m - 3 * e;
;     if (kind < 2) { const int kb = r / 112, nb = r - kb * 112, n0 = 32 * nb;
;         I.W = (kind == 0 ? wg : wu) + (size_t)e * DM * FF; I.WT = wsb + WS_WMGU + (size_t)e * 2 * FF * DM; I.K = DM; I.N = FF; I.drow0 = 256 * (n0 >> 7) + (n0 & 127) + (kind == 1 ? 128 : 0); I.k0 = 64 * kb; I.n0 = n0; I.scale = 16.f; }
;     else { const int kb = r >> 5, nb = r & 31, n0 = 32 * nb;
;         I.W = wd + (size_t)e * FF * DM; I.WT = wsb + WS_WMD + (size_t)e * DM * FF; I.K = FF; I.N = DM; I.drow0 = n0; I.k0 = 64 * kb; I.n0 = n0; I.scale = 32.f; }
; }
.LBB0_608:
	s_ashr_i32 s23, s22, 31
	v_lshrrev_b32_e32 v34, 3, v162
	s_lshl_b64 s[4:5], s[22:23], 2
	v_or_b32_e32 v62, s41, v34
	s_add_u32 s4, s12, s4
	v_lshlrev_b32_e32 v34, 4, v0
	s_addc_u32 s5, s13, s5
	v_and_b32_e32 v34, 0x70, v34
	v_mov_b32_e32 v35, 0
	v_lshl_add_u64 v[58:59], s[4:5], 0, v[34:35]
	v_mad_i64_i32 v[34:35], s[4:5], s14, v62, 0
	v_or_b32_e32 v36, 8, v62
	v_or_b32_e32 v42, 16, v62
	v_or_b32_e32 v44, 24, v62
	v_or_b32_e32 v50, 32, v62
	v_or_b32_e32 v52, 40, v62
	v_or_b32_e32 v60, 48, v62
	v_or_b32_e32 v62, 56, v62
	v_mad_i64_i32 v[36:37], s[4:5], s14, v36, 0
	v_mad_i64_i32 v[42:43], s[4:5], s14, v42, 0
	v_mad_i64_i32 v[44:45], s[4:5], s14, v44, 0
	v_mad_i64_i32 v[50:51], s[4:5], s14, v50, 0
	v_mad_i64_i32 v[52:53], s[4:5], s14, v52, 0
	v_mad_i64_i32 v[60:61], s[4:5], s14, v60, 0
	v_mad_i64_i32 v[62:63], s[4:5], s14, v62, 0
	v_lshl_add_u64 v[34:35], v[34:35], 2, v[58:59]
	v_lshl_add_u64 v[38:39], v[36:37], 2, v[58:59]
	v_lshl_add_u64 v[42:43], v[42:43], 2, v[58:59]
	v_lshl_add_u64 v[46:47], v[44:45], 2, v[58:59]
	v_lshl_add_u64 v[50:51], v[50:51], 2, v[58:59]
	v_lshl_add_u64 v[54:55], v[52:53], 2, v[58:59]
	v_lshl_add_u64 v[60:61], v[60:61], 2, v[58:59]
	v_lshl_add_u64 v[62:63], v[62:63], 2, v[58:59]
	global_load_dwordx4 v[34:37], v[34:35], off nt
	s_nop 0
	global_load_dwordx4 v[38:41], v[38:39], off nt
	s_nop 0
	global_load_dwordx4 v[42:45], v[42:43], off nt
	s_nop 0
	global_load_dwordx4 v[46:49], v[46:47], off nt
	s_nop 0
	global_load_dwordx4 v[50:53], v[50:51], off nt
	s_nop 0
	global_load_dwordx4 v[54:57], v[54:55], off nt
	s_nop 0
	global_load_dwordx4 v[58:61], v[60:61], off nt
	s_nop 0
	global_load_dwordx4 v[62:65], v[62:63], off nt
	s_cmpk_gt_i32 s32, 0x7fff
	s_cbranch_scc1 .LBB0_598
.LBB0_609:
	s_add_i32 s0, s32, 0x2800
	s_mul_hi_i32 s1, s0, 0x92492493
	s_add_i32 s1, s1, s0
	s_lshr_b32 s3, s1, 31
	s_ashr_i32 s1, s1, 10
	s_add_i32 s1, s1, s3
	s_mul_i32 s5, s1, 0xfffff900
	s_add_i32 s5, s5, s0
	s_mul_hi_i32 s0, s0, 0x30c30c31
	s_lshr_b32 s3, s0, 31
	s_ashr_i32 s4, s0, 10
	s_add_i32 s4, s4, s3
	s_mul_i32 s3, s4, -3
	s_add_i32 s3, s3, s1
	s_cmp_gt_i32 s3, 1
	s_mul_hi_i32 s7, s4, 0xe00000
	s_mul_i32 s25, s4, 0xe00000
	s_cbranch_scc0 .LBB0_612
	s_lshl_b32 s0, s32, 5
	s_and_b32 s44, s0, 0x3e0
	s_add_u32 s14, s60, s25
	s_addc_u32 s15, s61, s7
	s_mul_i32 s1, s4, 0x380000
	s_mul_hi_i32 s0, s4, 0x380000
	s_add_u32 s1, s34, s1
	s_addc_u32 s0, s35, s0
	s_add_u32 s12, s1, 0x7e00000
	s_addc_u32 s13, s0, 0
	s_lshl_b32 s0, s5, 1
	s_and_b32 s45, s0, 0xffffffc0
	s_cbranch_execz .LBB0_613
	s_mov_b32 s46, 0x42000000
	s_mov_b64 s[22:23], 0x400
	s_movk_i32 s47, 0xe00
	s_mov_b32 s24, s44
	s_branch .LBB0_614

; #define GAS __attribute__((address_space(1)))
; __device__ __forceinline__ void xf8_load(const float* W, int N, int k0, int n0, int lane, f32x4 (&v)[8]) {
; #pragma unroll
;     for (int i = 0; i < 8; ++i) v[i] = __builtin_nontemporal_load((const GAS f32x4*)(W + (size_t)(k0 + 8 * i + (lane >> 3)) * N + n0 + 4 * (lane & 7)));
; }
; __device__ __forceinline__ void moe_item(const float* wg, const float* wu, const float* wd, unsigned char* wsb, int it, MoeItem& I) {
;     const int m = it / 1792, r = it - m * 1792, e = m / 3, kind = m - 3 * e;
;     if (kind < 2) { const int kb = r / 112, nb = r - kb * 112, n0 = 32 * nb;
;         I.W = (kind == 0 ? wg : wu) + (size_t)e * DM * FF; I.WT = wsb + WS_WMGU + (size_t)e * 2 * FF * DM; I.K = DM; I.N = FF; I.drow0 = 256 * (n0 >> 7) + (n0 & 127) + (kind == 1 ? 128 : 0); I.k0 = 64 * kb; I.n0 = n0; I.scale = 16.f; }
;     else { const int kb = r >> 5, nb = r & 31, n0 = 32 * nb;
;         I.W = wd + (size_t)e * FF * DM; I.WT = wsb + WS_WMD + (size_t)e * DM * FF; I.K = FF; I.N = DM; I.drow0 = n0; I.k0 = 64 * kb; I.n0 = n0; I.scale = 32.f; }
; }
.LBB0_614:
	s_ashr_i32 s25, s24, 31
	v_lshrrev_b32_e32 v66, 3, v162
	s_lshl_b64 s[4:5], s[24:25], 2
	v_or_b32_e32 v94, s45, v66
	s_add_u32 s4, s14, s4
	v_lshlrev_b32_e32 v66, 4, v0
	s_addc_u32 s5, s15, s5
	v_and_b32_e32 v66, 0x70, v66
	v_mov_b32_e32 v67, 0
	v_lshl_add_u64 v[90:91], s[4:5], 0, v[66:67]
	v_mad_i64_i32 v[66:67], s[4:5], s22, v94, 0
	v_or_b32_e32 v68, 8, v94
	v_or_b32_e32 v74, 16, v94
	v_or_b32_e32 v76, 24, v94
	v_or_b32_e32 v82, 32, v94
	v_or_b32_e32 v84, 40, v94
	v_or_b32_e32 v92, 48, v94
	v_or_b32_e32 v94, 56, v94
	v_mad_i64_i32 v[68:69], s[4:5], s22, v68, 0
	v_mad_i64_i32 v[74:75], s[4:5], s22, v74, 0
	v_mad_i64_i32 v[76:77], s[4:5], s22, v76, 0
	v_mad_i64_i32 v[82:83], s[4:5], s22, v82, 0
	v_mad_i64_i32 v[84:85], s[4:5], s22, v84, 0
	v_mad_i64_i32 v[92:93], s[4:5], s22, v92, 0
	v_mad_i64_i32 v[94:95], s[4:5], s22, v94, 0
	v_lshl_add_u64 v[66:67], v[66:67], 2, v[90:91]
	v_lshl_add_u64 v[70:71], v[68:69], 2, v[90:91]
	v_lshl_add_u64 v[74:75], v[74:75], 2, v[90:91]
	v_lshl_add_u64 v[78:79], v[76:77], 2, v[90:91]
	v_lshl_add_u64 v[82:83], v[82:83], 2, v[90:91]
	v_lshl_add_u64 v[86:87], v[84:85], 2, v[90:91]
	v_lshl_add_u64 v[92:93], v[92:93], 2, v[90:91]
	v_lshl_add_u64 v[94:95], v[94:95], 2, v[90:91]
	global_load_dwordx4 v[66:69], v[66:67], off nt
	s_nop 0
	global_load_dwordx4 v[70:73], v[70:71], off nt
	s_nop 0
	global_load_dwordx4 v[74:77], v[74:75], off nt
	s_nop 0
	global_load_dwordx4 v[78:81], v[78:79], off nt
	s_nop 0
	global_load_dwordx4 v[82:85], v[82:83], off nt
	s_nop 0
	global_load_dwordx4 v[86:89], v[86:87], off nt
	s_nop 0
	global_load_dwordx4 v[90:93], v[92:93], off nt
	s_nop 0
	global_load_dwordx4 v[94:97], v[94:95], off nt
	s_cmpk_gt_i32 s32, 0x77ff
	s_cbranch_scc1 .LBB0_599
.LBB0_615:
	s_add_i32 s0, s32, 0x3000
	s_mul_hi_i32 s1, s0, 0x92492493
	s_add_i32 s1, s1, s0
	s_lshr_b32 s3, s1, 31
	s_ashr_i32 s1, s1, 10
	s_add_i32 s1, s1, s3
	s_mul_i32 s5, s1, 0xfffff900
	s_add_i32 s5, s5, s0
	s_mul_hi_i32 s0, s0, 0x30c30c31
	s_lshr_b32 s3, s0, 31
	s_ashr_i32 s4, s0, 10
	s_add_i32 s4, s4, s3
	s_mul_i32 s3, s4, -3
	s_add_i32 s3, s3, s1
	s_cmp_gt_i32 s3, 1
	s_mul_hi_i32 s7, s4, 0xe00000
	s_mul_i32 s31, s4, 0xe00000
	s_cbranch_scc0 .LBB0_618
	s_lshl_b32 s0, s32, 5
	s_and_b32 s48, s0, 0x3e0
	s_add_u32 s22, s60, s31
	s_addc_u32 s23, s61, s7
	s_mul_i32 s1, s4, 0x380000
	s_mul_hi_i32 s0, s4, 0x380000
	s_add_u32 s1, s34, s1
	s_addc_u32 s0, s35, s0
	s_add_u32 s14, s1, 0x7e00000
	s_addc_u32 s15, s0, 0
	s_lshl_b32 s0, s5, 1
	s_and_b32 s49, s0, 0xffffffc0
	s_cbranch_execz .LBB0_619
	s_mov_b32 s50, 0x42000000
	s_mov_b64 s[24:25], 0x400
	s_movk_i32 s51, 0xe00
	s_mov_b32 s30, s48
	s_branch .LBB0_620

; __device__ __forceinline__ unsigned pk4_fp8(float a, float b, float c, float d) { int w = 0; w = __builtin_amdgcn_cvt_pk_fp8_f32(a, b, w, false); w = __builtin_amdgcn_cvt_pk_fp8_f32(c, d, w, true); return (unsigned)w; }
; #define GAS __attribute__((address_space(1)))
; #define LAS __attribute__((address_space(3)))
; #define LDS_WAIT() asm volatile("s_waitcnt lgkmcnt(0)" ::: "memory")
; #define DEEP_LOAD(I, v, idx) do { if ((idx) < hi) { moe_item(wg, wu, wd, wsb, (idx), I); xf8_load(I.W, I.N, I.k0, I.n0, lane, v); } } while (0)
; #define DEEP_STEP(I, v, idx) do { if ((idx) < hi) { xf8_proc(v, I.K, I.WT, I.drow0, I.k0, I.scale, scr, lane); DEEP_LOAD(I, v, (idx) + 4 * stride); } } while (0)
; __device__ __forceinline__ void xf8_proc(const f32x4 (&v)[8], int K, unsigned char* WT, int drow0, int k0, float scale, LAS float* scr, int lane) {
; #pragma unroll
;     for (int i = 0; i < 8; ++i) { LAS float* d_ = scr + (8 * i + (lane >> 3)) * 33 + 4 * (lane & 7); d_[0] = v[i].x; d_[1] = v[i].y; d_[2] = v[i].z; d_[3] = v[i].w; }
;     LDS_WAIT(); asm volatile("" ::: "memory");
;     const int c = lane & 7;
; #pragma unroll
;     for (int j = 0; j < 4; ++j) { const int n = (lane >> 3) + 8 * j; const LAS float* s = scr + (8 * c) * 33 + n;
;         pg8::u32x2 o; o.x = pg8::pk4_fp8(s[0 * 33] * scale, s[1 * 33] * scale, s[2 * 33] * scale, s[3 * 33] * scale); o.y = pg8::pk4_fp8(s[4 * 33] * scale, s[5 * 33] * scale, s[6 * 33] * scale, s[7 * 33] * scale);
;         __builtin_nontemporal_store(o, (GAS pg8::u32x2*)(WT + (size_t)(drow0 + n) * K + k0 + 8 * c)); }
;     LDS_WAIT(); asm volatile("" ::: "memory");
; }
; __device__ __forceinline__ void moe_deep_items(const float* wg, const float* wu, const float* wd, unsigned char* wsb, int lo, int hi, int first, int stride, LAS float* scr, int lane) {
;     ...
;     DEEP_LOAD(I0, v0, it); DEEP_LOAD(I1, v1, it + stride); DEEP_LOAD(I2, v2, it + 2 * stride); DEEP_LOAD(I3, v3, it + 3 * stride);
;     for (; it < hi; it += 4 * stride) { DEEP_STEP(I0, v0, it); DEEP_STEP(I1, v1, it + stride); DEEP_STEP(I2, v2, it + 2 * stride); DEEP_STEP(I3, v3, it + 3 * stride); }
.LBB0_621:
	v_lshlrev_b32_e32 v130, 2, v0
	s_add_u32 s30, s34, 0x7e00000
	v_lshrrev_b32_e32 v131, 3, v162
	v_and_b32_e32 v130, 28, v130
	v_lshlrev_b32_e32 v132, 3, v0
	s_addc_u32 s31, s35, 0
	v_lshl_add_u32 v134, v130, 2, s72
	v_mul_u32_u24_e32 v140, 0x84, v131
	v_and_b32_e32 v132, 56, v132
	s_add_u32 s52, s34, 0x4600000
	v_mul_u32_u24_e32 v139, 0x84, v132
	v_mov_b32_e32 v135, 0
	v_lshlrev_b32_e32 v141, 2, v131
	s_addc_u32 s53, s35, 0
	s_lshl_b32 s0, s2, 4
	s_lshl_b32 s1, s82, 1
	v_add_u32_e32 v140, v134, v140
	v_or_b32_e32 v136, 8, v131
	v_or_b32_e32 v137, 16, v131
	v_or_b32_e32 v138, 24, v131
	v_mov_b32_e32 v133, v135
	v_add3_u32 v139, s72, v139, v141
	s_add_i32 s70, s32, 0x5000
	s_add_i32 s71, s0, s1
	s_addk_i32 s71, -4096
	s_lshl_b32 s74, s6, 5
	v_add_u32_e32 v141, 0x420, v140
	v_add_u32_e32 v142, 0x428, v140
	v_add_u32_e32 v143, 0x840, v140
	v_add_u32_e32 v144, 0x848, v140
	v_add_u32_e32 v145, 0xc60, v140
	v_add_u32_e32 v146, 0xc68, v140
	s_waitcnt lgkmcnt(0)
	v_add_u32_e32 v147, 0x1080, v140
	v_add_u32_e32 v148, 0x1088, v140
	v_add_u32_e32 v149, 0x14a0, v140
	v_add_u32_e32 v150, 0x14a8, v140
	v_add_u32_e32 v151, 0x18c0, v140
	v_add_u32_e32 v152, 0x18c8, v140
	v_add_u32_e32 v153, 0x1ce0, v140
	v_add_u32_e32 v154, 0x1ce8, v140
	s_branch .LBB0_625

; __device__ __forceinline__ void moe_item(const float* wg, const float* wu, const float* wd, unsigned char* wsb, int it, MoeItem& I) {
;     const int m = it / 1792, r = it - m * 1792, e = m / 3, kind = m - 3 * e;
;     if (kind < 2) { const int kb = r / 112, nb = r - kb * 112, n0 = 32 * nb;
;         I.W = (kind == 0 ? wg : wu) + (size_t)e * DM * FF; I.WT = wsb + WS_WMGU + (size_t)e * 2 * FF * DM; I.K = DM; I.N = FF; I.drow0 = 256 * (n0 >> 7) + (n0 & 127) + (kind == 1 ? 128 : 0); I.k0 = 64 * kb; I.n0 = n0; I.scale = 16.f; }
;     else { const int kb = r >> 5, nb = r & 31, n0 = 32 * nb;
;         I.W = wd + (size_t)e * FF * DM; I.WT = wsb + WS_WMD + (size_t)e * DM * FF; I.K = FF; I.N = DM; I.drow0 = n0; I.k0 = 64 * kb; I.n0 = n0; I.scale = 32.f; }
; }
; __global__ void __launch_bounds__(NTHREADS, 2) fwd(Args args) {
;     ...
;         if (conv_cls == 2) { moe_deep_items(args.in[18], args.in[19], args.in[20], ws, FILL1 + FILL2, MOE_ITEMS, gw, NGW, cscr, F.lane); __syncthreads(); }
.LBB0_704:
	s_add_i32 s32, s66, -2048
	s_add_i32 s6, s32, 0x1800
	s_cmp_lt_i32 s32, 0x9000
	s_cselect_b64 s[16:17], -1, 0
	s_cmp_gt_i32 s32, 0x8fff
	s_cbranch_scc1 .LBB0_708
	s_mul_hi_i32 s0, s6, 0x92492493
	s_add_i32 s0, s0, s6
	s_lshr_b32 s1, s0, 31
	s_ashr_i32 s0, s0, 10
	s_add_i32 s0, s0, s1
	s_mul_hi_i32 s1, s6, 0x30c30c31
	s_lshr_b32 s3, s1, 31
	s_ashr_i32 s4, s1, 10
	s_add_i32 s4, s4, s3
	s_mul_i32 s5, s0, 0xfffff900
	s_mul_i32 s3, s4, -3
	s_add_i32 s5, s5, s6
	s_add_i32 s3, s3, s0
	s_cmp_gt_i32 s3, 1
	s_mul_hi_i32 s7, s4, 0xe00000
	s_mul_i32 s15, s4, 0xe00000
	s_cbranch_scc0 .LBB0_712
	s_lshl_b32 s0, s32, 5
	s_and_b32 s36, s0, 0x3e0
	s_add_u32 s10, s60, s15
	s_addc_u32 s11, s61, s7
	s_mul_i32 s1, s4, 0x380000
	s_mul_hi_i32 s0, s4, 0x380000
	s_add_u32 s1, s34, s1
	s_addc_u32 s0, s35, s0
	s_add_u32 s8, s1, 0x7e00000
	s_addc_u32 s9, s0, 0
	s_lshl_b32 s0, s5, 1
	s_and_b32 s37, s0, 0xffffffc0
	s_cbranch_execz .LBB0_713
	s_mov_b32 s38, 0x42000000
	s_mov_b64 s[12:13], 0x400
	s_movk_i32 s39, 0xe00
	s_mov_b32 s14, s36
	s_branch .LBB0_714

; #define GAS __attribute__((address_space(1)))
; __device__ __forceinline__ void xf8_load(const float* W, int N, int k0, int n0, int lane, f32x4 (&v)[8]) {
; #pragma unroll
;     for (int i = 0; i < 8; ++i) v[i] = __builtin_nontemporal_load((const GAS f32x4*)(W + (size_t)(k0 + 8 * i + (lane >> 3)) * N + n0 + 4 * (lane & 7)));
; }
; __device__ __forceinline__ void moe_item(const float* wg, const float* wu, const float* wd, unsigned char* wsb, int it, MoeItem& I) {
;     const int m = it / 1792, r = it - m * 1792, e = m / 3, kind = m - 3 * e;
;     if (kind < 2) { const int kb = r / 112, nb = r - kb * 112, n0 = 32 * nb;
;         I.W = (kind == 0 ? wg : wu) + (size_t)e * DM * FF; I.WT = wsb + WS_WMGU + (size_t)e * 2 * FF * DM; I.K = DM; I.N = FF; I.drow0 = 256 * (n0 >> 7) + (n0 & 127) + (kind == 1 ? 128 : 0); I.k0 = 64 * kb; I.n0 = n0; I.scale = 16.f; }
;     else { const int kb = r >> 5, nb = r & 31, n0 = 32 * nb;
;         I.W = wd + (size_t)e * FF * DM; I.WT = wsb + WS_WMD + (size_t)e * DM * FF; I.K = FF; I.N = DM; I.drow0 = n0; I.k0 = 64 * kb; I.n0 = n0; I.scale = 32.f; }
; }
.LBB0_714:
	s_ashr_i32 s15, s14, 31
	v_lshrrev_b32_e32 v2, 3, v162
	s_lshl_b64 s[4:5], s[14:15], 2
	v_or_b32_e32 v30, s37, v2
	s_add_u32 s4, s10, s4
	v_lshlrev_b32_e32 v2, 4, v0
	s_addc_u32 s5, s11, s5
	v_and_b32_e32 v2, 0x70, v2
	v_mov_b32_e32 v3, 0
	v_lshl_add_u64 v[26:27], s[4:5], 0, v[2:3]
	v_mad_i64_i32 v[2:3], s[4:5], s12, v30, 0
	v_or_b32_e32 v4, 8, v30
	v_or_b32_e32 v10, 16, v30
	v_or_b32_e32 v12, 24, v30
	v_or_b32_e32 v18, 32, v30
	v_or_b32_e32 v20, 40, v30
	v_or_b32_e32 v28, 48, v30
	v_or_b32_e32 v30, 56, v30
	v_mad_i64_i32 v[4:5], s[4:5], s12, v4, 0
	v_mad_i64_i32 v[10:11], s[4:5], s12, v10, 0
	v_mad_i64_i32 v[12:13], s[4:5], s12, v12, 0
	v_mad_i64_i32 v[18:19], s[4:5], s12, v18, 0
	v_mad_i64_i32 v[20:21], s[4:5], s12, v20, 0
	v_mad_i64_i32 v[28:29], s[4:5], s12, v28, 0
	v_mad_i64_i32 v[30:31], s[4:5], s12, v30, 0
	v_lshl_add_u64 v[2:3], v[2:3], 2, v[26:27]
	v_lshl_add_u64 v[4:5], v[4:5], 2, v[26:27]
	v_lshl_add_u64 v[10:11], v[10:11], 2, v[26:27]
	v_lshl_add_u64 v[12:13], v[12:13], 2, v[26:27]
	v_lshl_add_u64 v[18:19], v[18:19], 2, v[26:27]
	v_lshl_add_u64 v[20:21], v[20:21], 2, v[26:27]
	v_lshl_add_u64 v[28:29], v[28:29], 2, v[26:27]
	v_lshl_add_u64 v[26:27], v[30:31], 2, v[26:27]
	global_load_dwordx4 v[6:9], v[2:3], off nt
	s_nop 0
	global_load_dwordx4 v[2:5], v[4:5], off nt
	s_nop 0
	global_load_dwordx4 v[14:17], v[10:11], off nt
	s_nop 0
	global_load_dwordx4 v[10:13], v[12:13], off nt
	s_nop 0
	global_load_dwordx4 v[22:25], v[18:19], off nt
	s_nop 0
	global_load_dwordx4 v[18:21], v[20:21], off nt
	s_nop 0
	global_load_dwordx4 v[30:33], v[28:29], off nt
	s_nop 0
	global_load_dwordx4 v[26:29], v[26:27], off nt
	s_cmp_gt_i32 s32, 0x87ff
	s_cbranch_scc1 .LBB0_709

; __device__ __forceinline__ unsigned pk4_fp8(float a, float b, float c, float d) { int w = 0; w = __builtin_amdgcn_cvt_pk_fp8_f32(a, b, w, false); w = __builtin_amdgcn_cvt_pk_fp8_f32(c, d, w, true); return (unsigned)w; }
; #define GAS __attribute__((address_space(1)))
; #define LAS __attribute__((address_space(3)))
; #define LDS_WAIT() asm volatile("s_waitcnt lgkmcnt(0)" ::: "memory")
; #define DEEP_LOAD(I, v, idx) do { if ((idx) < hi) { moe_item(wg, wu, wd, wsb, (idx), I); xf8_load(I.W, I.N, I.k0, I.n0, lane, v); } } while (0)
; #define DEEP_STEP(I, v, idx) do { if ((idx) < hi) { xf8_proc(v, I.K, I.WT, I.drow0, I.k0, I.scale, scr, lane); DEEP_LOAD(I, v, (idx) + 4 * stride); } } while (0)
; __device__ __forceinline__ void xf8_proc(const f32x4 (&v)[8], int K, unsigned char* WT, int drow0, int k0, float scale, LAS float* scr, int lane) {
; #pragma unroll
;     for (int i = 0; i < 8; ++i) { LAS float* d_ = scr + (8 * i + (lane >> 3)) * 33 + 4 * (lane & 7); d_[0] = v[i].x; d_[1] = v[i].y; d_[2] = v[i].z; d_[3] = v[i].w; }
;     LDS_WAIT(); asm volatile("" ::: "memory");
;     const int c = lane & 7;
; #pragma unroll
;     for (int j = 0; j < 4; ++j) { const int n = (lane >> 3) + 8 * j; const LAS float* s = scr + (8 * c) * 33 + n;
;         pg8::u32x2 o; o.x = pg8::pk4_fp8(s[0 * 33] * scale, s[1 * 33] * scale, s[2 * 33] * scale, s[3 * 33] * scale); o.y = pg8::pk4_fp8(s[4 * 33] * scale, s[5 * 33] * scale, s[6 * 33] * scale, s[7 * 33] * scale);
;         __builtin_nontemporal_store(o, (GAS pg8::u32x2*)(WT + (size_t)(drow0 + n) * K + k0 + 8 * c)); }
;     LDS_WAIT(); asm volatile("" ::: "memory");
; }
; __device__ __forceinline__ void moe_deep_items(const float* wg, const float* wu, const float* wd, unsigned char* wsb, int lo, int hi, int first, int stride, LAS float* scr, int lane) {
;     ...
;     DEEP_LOAD(I0, v0, it); DEEP_LOAD(I1, v1, it + stride); DEEP_LOAD(I2, v2, it + 2 * stride); DEEP_LOAD(I3, v3, it + 3 * stride);
;     for (; it < hi; it += 4 * stride) { DEEP_STEP(I0, v0, it); DEEP_STEP(I1, v1, it + stride); DEEP_STEP(I2, v2, it + 2 * stride); DEEP_STEP(I3, v3, it + 3 * stride); }
.LBB0_733:
	v_lshlrev_b32_e32 v130, 2, v0
	s_add_u32 s30, s34, 0x7e00000
	v_lshrrev_b32_e32 v131, 3, v162
	v_and_b32_e32 v130, 28, v130
	v_lshlrev_b32_e32 v132, 3, v0
	s_addc_u32 s31, s35, 0
	v_lshl_add_u32 v134, v130, 2, s72
	v_mul_u32_u24_e32 v140, 0x84, v131
	v_and_b32_e32 v132, 56, v132
	s_add_u32 s52, s34, 0x4600000
	v_mul_u32_u24_e32 v139, 0x84, v132
	v_mov_b32_e32 v135, 0
	v_lshlrev_b32_e32 v141, 2, v131
	s_addc_u32 s53, s35, 0
	s_lshl_b32 s0, s2, 4
	s_lshl_b32 s1, s82, 1
	v_add_u32_e32 v140, v134, v140
	v_or_b32_e32 v136, 8, v131
	v_or_b32_e32 v137, 16, v131
	v_or_b32_e32 v138, 24, v131
	v_mov_b32_e32 v133, v135
	v_add3_u32 v139, s72, v139, v141
	s_add_i32 s70, s32, 0x5000
	s_add_i32 s71, s0, s1
	s_addk_i32 s71, -4096
	s_lshl_b32 s72, s6, 5
	v_add_u32_e32 v141, 0x420, v140
	v_add_u32_e32 v142, 0x428, v140
	v_add_u32_e32 v143, 0x840, v140
	v_add_u32_e32 v144, 0x848, v140
	v_add_u32_e32 v145, 0xc60, v140
	v_add_u32_e32 v146, 0xc68, v140
	s_waitcnt lgkmcnt(0)
	v_add_u32_e32 v147, 0x1080, v140
	v_add_u32_e32 v148, 0x1088, v140
	v_add_u32_e32 v149, 0x14a0, v140
	v_add_u32_e32 v150, 0x14a8, v140
	v_add_u32_e32 v151, 0x18c0, v140
	v_add_u32_e32 v152, 0x18c8, v140
	v_add_u32_e32 v153, 0x1ce0, v140
	v_add_u32_e32 v154, 0x1ce8, v140
	s_branch .LBB0_737

; #define LAS __attribute__((address_space(3)))
; __device__ __forceinline__ void moe_item(const float* wg, const float* wu, const float* wd, unsigned char* wsb, int it, MoeItem& I) {
;     const int m = it / 1792, r = it - m * 1792, e = m / 3, kind = m - 3 * e;
;     if (kind < 2) { const int kb = r / 112, nb = r - kb * 112, n0 = 32 * nb;
;         I.W = (kind == 0 ? wg : wu) + (size_t)e * DM * FF; I.WT = wsb + WS_WMGU + (size_t)e * 2 * FF * DM; I.K = DM; I.N = FF; I.drow0 = 256 * (n0 >> 7) + (n0 & 127) + (kind == 1 ? 128 : 0); I.k0 = 64 * kb; I.n0 = n0; I.scale = 16.f; }
;     else { const int kb = r >> 5, nb = r & 31, n0 = 32 * nb;
;         I.W = wd + (size_t)e * FF * DM; I.WT = wsb + WS_WMD + (size_t)e * DM * FF; I.K = FF; I.N = DM; I.drow0 = n0; I.k0 = 64 * kb; I.n0 = n0; I.scale = 32.f; }
; }
; __global__ void __launch_bounds__(NTHREADS, 2) fwd(Args args) {
;     ...
;         if (F.bid >= 128) moe_deep_items(args.in[18], args.in[19], args.in[20], ws, FILL1, FILL1 + FILL2, (F.bid - 128) * NWAVES + F.wave, 128 * NWAVES, (LAS float*)(F.lds + RING_OFF + F.wave * 16384), F.lane);
.LBB0_809:
	s_cmpk_lt_i32 s2, 0x80
	s_cbranch_scc1 .LBB0_872
	s_add_i32 s6, s66, 0xfffffc00
	s_cmpk_lt_i32 s6, 0x1000
	s_cselect_b64 s[18:19], -1, 0
	s_cmpk_gt_i32 s6, 0xfff
	s_cbranch_scc1 .LBB0_814
	s_mul_hi_i32 s0, s6, 0x92492493
	s_add_i32 s0, s0, s6
	s_lshr_b32 s1, s0, 31
	s_ashr_i32 s0, s0, 10
	s_add_i32 s0, s0, s1
	s_mul_hi_i32 s1, s6, 0x30c30c31
	s_lshr_b32 s3, s1, 31
	s_ashr_i32 s4, s1, 10
	s_add_i32 s4, s4, s3
	s_mul_i32 s5, s0, 0xfffff900
	s_mul_i32 s3, s4, -3
	s_add_i32 s5, s5, s6
	s_add_i32 s3, s3, s0
	s_cmp_gt_i32 s3, 1
	s_mul_hi_i32 s7, s4, 0xe00000
	s_mul_i32 s17, s4, 0xe00000
	s_cbranch_scc0 .LBB0_818
	s_lshl_b32 s0, s6, 5
	s_and_b32 s36, s0, 0x3e0
	s_add_u32 s14, s60, s17
	s_addc_u32 s15, s61, s7
	s_mul_i32 s1, s4, 0x380000
	s_mul_hi_i32 s0, s4, 0x380000
	s_add_u32 s1, s34, s1
	s_addc_u32 s0, s35, s0
	s_add_u32 s8, s1, 0x7e00000
	s_addc_u32 s9, s0, 0
	s_lshl_b32 s0, s5, 1
	s_and_b32 s37, s0, 0xffffffc0
	s_cbranch_execz .LBB0_819
	s_mov_b32 s38, 0x42000000
	s_mov_b64 s[12:13], 0x400
	s_movk_i32 s39, 0xe00
	s_mov_b32 s16, s36
	s_branch .LBB0_820
.LBB0_814:
	v_mov_b32_e32 v29, 0
	v_mov_b32_e32 v28, v29
	v_mov_b32_e32 v27, v29
	v_mov_b32_e32 v26, v29
	v_mov_b32_e32 v33, v29
	v_mov_b32_e32 v32, v29
	v_mov_b32_e32 v31, v29
	v_mov_b32_e32 v30, v29
	v_mov_b32_e32 v21, v29
	v_mov_b32_e32 v20, v29
	v_mov_b32_e32 v19, v29
	v_mov_b32_e32 v18, v29
	v_mov_b32_e32 v25, v29
	v_mov_b32_e32 v24, v29
	v_mov_b32_e32 v23, v29
	v_mov_b32_e32 v22, v29
	v_mov_b32_e32 v13, v29
	v_mov_b32_e32 v12, v29
	v_mov_b32_e32 v11, v29
	v_mov_b32_e32 v10, v29
	v_mov_b32_e32 v17, v29
	v_mov_b32_e32 v16, v29
	v_mov_b32_e32 v15, v29
	v_mov_b32_e32 v14, v29
	v_mov_b32_e32 v5, v29
	v_mov_b32_e32 v4, v29
	v_mov_b32_e32 v3, v29
	v_mov_b32_e32 v2, v29
	v_mov_b32_e32 v9, v29
	v_mov_b32_e32 v8, v29
	v_mov_b32_e32 v7, v29
	v_mov_b32_e32 v6, v29
	s_cmpk_gt_i32 s66, 0xfff
	s_cbranch_scc0 .LBB0_821
.LBB0_815:
	s_cmpk_gt_i32 s6, 0x7ff
	s_cbranch_scc0 .LBB0_827
.LBB0_816:
	s_cmpk_gt_i32 s6, 0x3ff
	s_cbranch_scc0 .LBB0_833

; #define GAS __attribute__((address_space(1)))
; __device__ __forceinline__ void xf8_load(const float* W, int N, int k0, int n0, int lane, f32x4 (&v)[8]) {
; #pragma unroll
;     for (int i = 0; i < 8; ++i) v[i] = __builtin_nontemporal_load((const GAS f32x4*)(W + (size_t)(k0 + 8 * i + (lane >> 3)) * N + n0 + 4 * (lane & 7)));
; }
.LBB0_820:
	s_ashr_i32 s17, s16, 31
	v_lshrrev_b32_e32 v2, 3, v162
	s_lshl_b64 s[4:5], s[16:17], 2
	v_or_b32_e32 v30, s37, v2
	s_add_u32 s4, s14, s4
	v_lshlrev_b32_e32 v2, 4, v0
	s_addc_u32 s5, s15, s5
	v_and_b32_e32 v2, 0x70, v2
	v_mov_b32_e32 v3, 0
	v_lshl_add_u64 v[26:27], s[4:5], 0, v[2:3]
	v_mad_i64_i32 v[2:3], s[4:5], s12, v30, 0
	v_lshl_add_u64 v[10:11], v[2:3], 2, v[26:27]
	v_or_b32_e32 v2, 8, v30
	v_mad_i64_i32 v[2:3], s[4:5], s12, v2, 0
	v_lshl_add_u64 v[12:13], v[2:3], 2, v[26:27]
	global_load_dwordx4 v[6:9], v[10:11], off nt
	global_load_dwordx4 v[2:5], v[12:13], off nt
	v_or_b32_e32 v10, 16, v30
	v_or_b32_e32 v12, 24, v30
	v_or_b32_e32 v18, 32, v30
	v_or_b32_e32 v20, 40, v30
	v_or_b32_e32 v28, 48, v30
	v_or_b32_e32 v30, 56, v30
	v_mad_i64_i32 v[10:11], s[4:5], s12, v10, 0
	v_mad_i64_i32 v[12:13], s[4:5], s12, v12, 0
	v_mad_i64_i32 v[18:19], s[4:5], s12, v18, 0
	v_mad_i64_i32 v[20:21], s[4:5], s12, v20, 0
	v_mad_i64_i32 v[28:29], s[4:5], s12, v28, 0
	v_mad_i64_i32 v[30:31], s[4:5], s12, v30, 0
	v_lshl_add_u64 v[10:11], v[10:11], 2, v[26:27]
	v_lshl_add_u64 v[12:13], v[12:13], 2, v[26:27]
	v_lshl_add_u64 v[18:19], v[18:19], 2, v[26:27]
	v_lshl_add_u64 v[20:21], v[20:21], 2, v[26:27]
	v_lshl_add_u64 v[28:29], v[28:29], 2, v[26:27]
	v_lshl_add_u64 v[26:27], v[30:31], 2, v[26:27]
	global_load_dwordx4 v[14:17], v[10:11], off nt
	s_nop 0
	global_load_dwordx4 v[10:13], v[12:13], off nt
	s_nop 0
	global_load_dwordx4 v[22:25], v[18:19], off nt
	s_nop 0
	global_load_dwordx4 v[18:21], v[20:21], off nt
	s_nop 0
	global_load_dwordx4 v[30:33], v[28:29], off nt
	s_nop 0
	global_load_dwordx4 v[26:29], v[26:27], off nt
	s_cmpk_gt_i32 s66, 0xfff
	s_cbranch_scc1 .LBB0_815

; #define GAS __attribute__((address_space(1)))
; __device__ __forceinline__ void xf8_load(const float* W, int N, int k0, int n0, int lane, f32x4 (&v)[8]) {
; #pragma unroll
;     for (int i = 0; i < 8; ++i) v[i] = __builtin_nontemporal_load((const GAS f32x4*)(W + (size_t)(k0 + 8 * i + (lane >> 3)) * N + n0 + 4 * (lane & 7)));
; }
.LBB0_826:
	s_ashr_i32 s23, s22, 31
	v_lshrrev_b32_e32 v34, 3, v162
	s_lshl_b64 s[4:5], s[22:23], 2
	v_or_b32_e32 v62, s41, v34
	s_add_u32 s4, s14, s4
	v_lshlrev_b32_e32 v34, 4, v0
	s_addc_u32 s5, s15, s5
	v_and_b32_e32 v34, 0x70, v34
	v_mov_b32_e32 v35, 0
	v_lshl_add_u64 v[58:59], s[4:5], 0, v[34:35]
	v_mad_i64_i32 v[34:35], s[4:5], s16, v62, 0
	v_or_b32_e32 v36, 8, v62
	v_or_b32_e32 v42, 16, v62
	v_or_b32_e32 v44, 24, v62
	v_or_b32_e32 v50, 32, v62
	v_or_b32_e32 v52, 40, v62
	v_or_b32_e32 v60, 48, v62
	v_or_b32_e32 v62, 56, v62
	v_mad_i64_i32 v[36:37], s[4:5], s16, v36, 0
	v_mad_i64_i32 v[42:43], s[4:5], s16, v42, 0
	v_mad_i64_i32 v[44:45], s[4:5], s16, v44, 0
	v_mad_i64_i32 v[50:51], s[4:5], s16, v50, 0
	v_mad_i64_i32 v[52:53], s[4:5], s16, v52, 0
	v_mad_i64_i32 v[60:61], s[4:5], s16, v60, 0
	v_mad_i64_i32 v[62:63], s[4:5], s16, v62, 0
	v_lshl_add_u64 v[34:35], v[34:35], 2, v[58:59]
	v_lshl_add_u64 v[38:39], v[36:37], 2, v[58:59]
	v_lshl_add_u64 v[42:43], v[42:43], 2, v[58:59]
	v_lshl_add_u64 v[46:47], v[44:45], 2, v[58:59]
	v_lshl_add_u64 v[50:51], v[50:51], 2, v[58:59]
	v_lshl_add_u64 v[54:55], v[52:53], 2, v[58:59]
	v_lshl_add_u64 v[60:61], v[60:61], 2, v[58:59]
	v_lshl_add_u64 v[62:63], v[62:63], 2, v[58:59]
	global_load_dwordx4 v[34:37], v[34:35], off nt
	s_nop 0
	global_load_dwordx4 v[38:41], v[38:39], off nt
	s_nop 0
	global_load_dwordx4 v[42:45], v[42:43], off nt
	s_nop 0
	global_load_dwordx4 v[46:49], v[46:47], off nt
	s_nop 0
	global_load_dwordx4 v[50:53], v[50:51], off nt
	s_nop 0
	global_load_dwordx4 v[54:57], v[54:55], off nt
	s_nop 0
	global_load_dwordx4 v[58:61], v[60:61], off nt
	s_nop 0
	global_load_dwordx4 v[62:65], v[62:63], off nt
	s_cmpk_gt_i32 s6, 0x7ff
	s_cbranch_scc1 .LBB0_816

; #define GAS __attribute__((address_space(1)))
; __device__ __forceinline__ void xf8_load(const float* W, int N, int k0, int n0, int lane, f32x4 (&v)[8]) {
; #pragma unroll
;     for (int i = 0; i < 8; ++i) v[i] = __builtin_nontemporal_load((const GAS f32x4*)(W + (size_t)(k0 + 8 * i + (lane >> 3)) * N + n0 + 4 * (lane & 7)));
; }
.LBB0_832:
	s_ashr_i32 s25, s24, 31
	v_lshrrev_b32_e32 v66, 3, v162
	s_lshl_b64 s[4:5], s[24:25], 2
	v_or_b32_e32 v94, s45, v66
	s_add_u32 s4, s16, s4
	v_lshlrev_b32_e32 v66, 4, v0
	s_addc_u32 s5, s17, s5
	v_and_b32_e32 v66, 0x70, v66
	v_mov_b32_e32 v67, 0
	v_lshl_add_u64 v[90:91], s[4:5], 0, v[66:67]
	v_mad_i64_i32 v[66:67], s[4:5], s22, v94, 0
	v_or_b32_e32 v68, 8, v94
	v_or_b32_e32 v74, 16, v94
	v_or_b32_e32 v76, 24, v94
	v_or_b32_e32 v82, 32, v94
	v_or_b32_e32 v84, 40, v94
	v_or_b32_e32 v92, 48, v94
	v_or_b32_e32 v94, 56, v94
	v_mad_i64_i32 v[68:69], s[4:5], s22, v68, 0
	v_mad_i64_i32 v[74:75], s[4:5], s22, v74, 0
	v_mad_i64_i32 v[76:77], s[4:5], s22, v76, 0
	v_mad_i64_i32 v[82:83], s[4:5], s22, v82, 0
	v_mad_i64_i32 v[84:85], s[4:5], s22, v84, 0
	v_mad_i64_i32 v[92:93], s[4:5], s22, v92, 0
	v_mad_i64_i32 v[94:95], s[4:5], s22, v94, 0
	v_lshl_add_u64 v[66:67], v[66:67], 2, v[90:91]
	v_lshl_add_u64 v[70:71], v[68:69], 2, v[90:91]
	v_lshl_add_u64 v[74:75], v[74:75], 2, v[90:91]
	v_lshl_add_u64 v[78:79], v[76:77], 2, v[90:91]
	v_lshl_add_u64 v[82:83], v[82:83], 2, v[90:91]
	v_lshl_add_u64 v[86:87], v[84:85], 2, v[90:91]
	v_lshl_add_u64 v[92:93], v[92:93], 2, v[90:91]
	v_lshl_add_u64 v[94:95], v[94:95], 2, v[90:91]
	global_load_dwordx4 v[66:69], v[66:67], off nt
	s_nop 0
	global_load_dwordx4 v[70:73], v[70:71], off nt
	s_nop 0
	global_load_dwordx4 v[74:77], v[74:75], off nt
	s_nop 0
	global_load_dwordx4 v[78:81], v[78:79], off nt
	s_nop 0
	global_load_dwordx4 v[82:85], v[82:83], off nt
	s_nop 0
	global_load_dwordx4 v[86:89], v[86:87], off nt
	s_nop 0
	global_load_dwordx4 v[90:93], v[92:93], off nt
	s_nop 0
	global_load_dwordx4 v[94:97], v[94:95], off nt
	s_cmpk_gt_i32 s6, 0x3ff
	s_cbranch_scc1 .LBB0_817

; __device__ __forceinline__ unsigned pk4_fp8(float a, float b, float c, float d) { int w = 0; w = __builtin_amdgcn_cvt_pk_fp8_f32(a, b, w, false); w = __builtin_amdgcn_cvt_pk_fp8_f32(c, d, w, true); return (unsigned)w; }
; #define GAS __attribute__((address_space(1)))
; #define LAS __attribute__((address_space(3)))
; #define LDS_WAIT() asm volatile("s_waitcnt lgkmcnt(0)" ::: "memory")
; #define DEEP_LOAD(I, v, idx) do { if ((idx) < hi) { moe_item(wg, wu, wd, wsb, (idx), I); xf8_load(I.W, I.N, I.k0, I.n0, lane, v); } } while (0)
; #define DEEP_STEP(I, v, idx) do { if ((idx) < hi) { xf8_proc(v, I.K, I.WT, I.drow0, I.k0, I.scale, scr, lane); DEEP_LOAD(I, v, (idx) + 4 * stride); } } while (0)
; __device__ __forceinline__ void xf8_proc(const f32x4 (&v)[8], int K, unsigned char* WT, int drow0, int k0, float scale, LAS float* scr, int lane) {
; #pragma unroll
;     for (int i = 0; i < 8; ++i) { LAS float* d_ = scr + (8 * i + (lane >> 3)) * 33 + 4 * (lane & 7); d_[0] = v[i].x; d_[1] = v[i].y; d_[2] = v[i].z; d_[3] = v[i].w; }
;     LDS_WAIT(); asm volatile("" ::: "memory");
;     const int c = lane & 7;
; #pragma unroll
;     for (int j = 0; j < 4; ++j) { const int n = (lane >> 3) + 8 * j; const LAS float* s = scr + (8 * c) * 33 + n;
;         pg8::u32x2 o; o.x = pg8::pk4_fp8(s[0 * 33] * scale, s[1 * 33] * scale, s[2 * 33] * scale, s[3 * 33] * scale); o.y = pg8::pk4_fp8(s[4 * 33] * scale, s[5 * 33] * scale, s[6 * 33] * scale, s[7 * 33] * scale);
;         __builtin_nontemporal_store(o, (GAS pg8::u32x2*)(WT + (size_t)(drow0 + n) * K + k0 + 8 * c)); }
;     LDS_WAIT(); asm volatile("" ::: "memory");
; }
; __device__ __forceinline__ void moe_deep_items(const float* wg, const float* wu, const float* wd, unsigned char* wsb, int lo, int hi, int first, int stride, LAS float* scr, int lane) {
;     ...
;     DEEP_LOAD(I0, v0, it); DEEP_LOAD(I1, v1, it + stride); DEEP_LOAD(I2, v2, it + 2 * stride); DEEP_LOAD(I3, v3, it + 3 * stride);
;     for (; it < hi; it += 4 * stride) { DEEP_STEP(I0, v0, it); DEEP_STEP(I1, v1, it + stride); DEEP_STEP(I2, v2, it + 2 * stride); DEEP_STEP(I3, v3, it + 3 * stride); }
.LBB0_842:
	s_addk_i32 s70, 0x1000
	s_addk_i32 s71, 0x2000
	s_add_i32 s72, s72, 0x20000
	s_cmpk_lt_i32 s73, 0x0
	s_cbranch_scc0 .LBB0_872
.LBB0_843:
	s_waitcnt vmcnt(0)
	ds_write2_b32 v140, v6, v7 offset1:1
	ds_write2_b32 v140, v8, v9 offset0:2 offset1:3
	ds_write2_b32 v141, v2, v3 offset1:1
	ds_write2_b32 v142, v4, v5 offset1:1
	ds_write2_b32 v143, v14, v15 offset1:1
	ds_write2_b32 v144, v16, v17 offset1:1
	ds_write2_b32 v145, v10, v11 offset1:1
	ds_write2_b32 v146, v12, v13 offset1:1
	ds_write2_b32 v147, v22, v23 offset1:1
	ds_write2_b32 v148, v24, v25 offset1:1
	ds_write2_b32 v149, v18, v19 offset1:1
	ds_write2_b32 v150, v20, v21 offset1:1
	ds_write2_b32 v151, v30, v31 offset1:1
	ds_write2_b32 v152, v32, v33 offset1:1
	ds_write2_b32 v153, v26, v27 offset1:1
	ds_write2_b32 v154, v28, v29 offset1:1
	s_waitcnt lgkmcnt(0)
	ds_read2_b32 v[156:157], v139 offset1:8
	ds_read2_b32 v[158:159], v139 offset0:33 offset1:41
	ds_read2_b32 v[160:161], v139 offset0:66 offset1:74
	ds_read2_b32 v[168:169], v139 offset0:99 offset1:107
	ds_read2_b32 v[170:171], v139 offset0:132 offset1:140
	ds_read2_b32 v[172:173], v139 offset0:165 offset1:173
	v_mov_b32_e32 v174, 0
	s_waitcnt lgkmcnt(5)
	v_mul_f32_e32 v134, s38, v156
	s_waitcnt lgkmcnt(4)
	v_mul_f32_e32 v155, s38, v158
	ds_read2_b32 v[176:177], v139 offset0:198 offset1:206
	ds_read2_b32 v[178:179], v139 offset0:231 offset1:239
	v_cvt_pk_fp8_f32 v174, v134, v155
	s_waitcnt lgkmcnt(3)
	v_mul_f32_e32 v134, s38, v170
	s_waitcnt lgkmcnt(2)
	v_mul_f32_e32 v155, s38, v172
	v_mov_b32_e32 v175, 0
	v_cvt_pk_fp8_f32 v175, v134, v155
	s_add_i32 s73, s70, 0xffffe400
	s_ashr_i32 s0, s37, 31
	s_add_u32 s4, s8, s37
	s_addc_u32 s5, s9, s0
	s_waitcnt lgkmcnt(1)
	v_mul_f32_e32 v134, s38, v176
	s_waitcnt lgkmcnt(0)
	v_mul_f32_e32 v155, s38, v178
	v_lshl_add_u64 v[166:167], s[4:5], 0, v[132:133]
	v_mul_f32_e32 v156, s38, v160
	v_mul_f32_e32 v158, s38, v168
	v_cvt_pk_fp8_f32 v175, v134, v155 op_sel:[0,0,1]
	v_add_u32_e32 v134, s36, v131
	v_cvt_pk_fp8_f32 v174, v156, v158 op_sel:[0,0,1]
	v_mad_i64_i32 v[180:181], s[4:5], v134, s39, v[166:167]
	v_mul_f32_e32 v134, s38, v157
	v_mul_f32_e32 v155, s38, v159
	v_mov_b32_e32 v156, 0
	v_cvt_pk_fp8_f32 v156, v134, v155
	v_mul_f32_e32 v134, s38, v171
	v_mul_f32_e32 v155, s38, v173
	v_mov_b32_e32 v157, 0
	v_cvt_pk_fp8_f32 v157, v134, v155
	v_mul_f32_e32 v158, s38, v161
	v_mul_f32_e32 v159, s38, v169
	v_mul_f32_e32 v134, s38, v177
	v_mul_f32_e32 v155, s38, v179
	v_cvt_pk_fp8_f32 v156, v158, v159 op_sel:[0,0,1]
	v_cvt_pk_fp8_f32 v157, v134, v155 op_sel:[0,0,1]
	v_add_u32_e32 v134, s36, v136
	global_store_dwordx2 v[180:181], v[174:175], off nt
	v_mad_i64_i32 v[160:161], s[4:5], v134, s39, v[166:167]
	ds_read2_b32 v[158:159], v139 offset0:16 offset1:24
	ds_read2_b32 v[168:169], v139 offset0:49 offset1:57
	ds_read2_b32 v[170:171], v139 offset0:82 offset1:90
	global_store_dwordx2 v[160:161], v[156:157], off nt
	ds_read2_b32 v[156:157], v139 offset0:115 offset1:123
	ds_read2_b32 v[160:161], v139 offset0:148 offset1:156
	ds_read2_b32 v[172:173], v139 offset0:181 offset1:189
	s_waitcnt lgkmcnt(5)
	v_mul_f32_e32 v134, s38, v158
	s_waitcnt lgkmcnt(4)
	v_mul_f32_e32 v155, s38, v168
	v_mov_b32_e32 v174, 0
	ds_read2_b32 v[176:177], v139 offset0:214 offset1:222
	ds_read2_b32 v[178:179], v139 offset0:247 offset1:255
	v_cvt_pk_fp8_f32 v174, v134, v155
	s_waitcnt lgkmcnt(3)
	v_mul_f32_e32 v134, s38, v160
	s_waitcnt lgkmcnt(2)
	v_mul_f32_e32 v155, s38, v172
	v_mov_b32_e32 v175, 0
	v_cvt_pk_fp8_f32 v175, v134, v155
	s_waitcnt lgkmcnt(1)
	v_mul_f32_e32 v134, s38, v176
	s_waitcnt lgkmcnt(0)
	v_mul_f32_e32 v155, s38, v178
	v_mul_f32_e32 v158, s38, v170
	v_mul_f32_e32 v156, s38, v156
	v_cvt_pk_fp8_f32 v175, v134, v155 op_sel:[0,0,1]
	v_add_u32_e32 v134, s36, v137
	v_cvt_pk_fp8_f32 v174, v158, v156 op_sel:[0,0,1]
	v_mad_i64_i32 v[180:181], s[4:5], v134, s39, v[166:167]
	v_mul_f32_e32 v134, s38, v159
	v_mul_f32_e32 v155, s38, v169
	v_mov_b32_e32 v156, 0
	v_mul_f32_e32 v159, s38, v157
	v_cvt_pk_fp8_f32 v156, v134, v155
	v_mul_f32_e32 v134, s38, v161
	v_mul_f32_e32 v155, s38, v173
	v_mov_b32_e32 v157, 0
	v_cvt_pk_fp8_f32 v157, v134, v155
	v_mul_f32_e32 v158, s38, v171
	v_mul_f32_e32 v134, s38, v177
	v_mul_f32_e32 v155, s38, v179
	v_cvt_pk_fp8_f32 v156, v158, v159 op_sel:[0,0,1]
	v_cvt_pk_fp8_f32 v157, v134, v155 op_sel:[0,0,1]
	v_add_u32_e32 v134, s36, v138
	v_mad_i64_i32 v[158:159], s[4:5], v134, s39, v[166:167]
	global_store_dwordx2 v[180:181], v[174:175], off nt
	global_store_dwordx2 v[158:159], v[156:157], off nt
	s_waitcnt lgkmcnt(0)
	s_cmpk_gt_i32 s73, -1
	s_cbranch_scc1 .LBB0_850
	s_add_i32 s0, s70, 0xfffff400
	s_mul_hi_i32 s1, s0, 0x92492493
	s_add_i32 s1, s1, s0
	s_mul_hi_i32 s0, s0, 0x30c30c31
	s_lshr_b32 s3, s1, 31
	s_ashr_i32 s5, s1, 10
	s_lshr_b32 s1, s0, 31
	s_ashr_i32 s4, s0, 10
	s_add_i32 s4, s4, s1
	s_add_i32 s5, s5, s3
	s_mul_i32 s3, s4, -3
	s_add_i32 s3, s3, s5
	s_mov_b64 s[22:23], -1
	s_cmp_gt_i32 s3, 1
	s_mul_hi_i32 s6, s4, 0xe00000
	s_mul_i32 s7, s4, 0xe00000
	s_cbranch_scc0 .LBB0_846
	s_and_b32 s36, s72, 0x3e0
	s_add_u32 s18, s60, s7
	s_addc_u32 s19, s61, s6
	s_mul_i32 s1, s4, 0x380000
	s_mul_hi_i32 s0, s4, 0x380000
	s_add_u32 s8, s30, s1
	s_addc_u32 s9, s31, s0
	s_mul_i32 s0, s5, 0xfffff200
	s_add_i32 s0, s71, s0
	s_addk_i32 s0, 0x1800
	s_and_b32 s37, s0, 0xffffffc0
	s_mov_b64 s[22:23], 0

; __device__ __forceinline__ unsigned pk4_fp8(float a, float b, float c, float d) { int w = 0; w = __builtin_amdgcn_cvt_pk_fp8_f32(a, b, w, false); w = __builtin_amdgcn_cvt_pk_fp8_f32(c, d, w, true); return (unsigned)w; }
; #define GAS __attribute__((address_space(1)))
; #define LAS __attribute__((address_space(3)))
; #define LDS_WAIT() asm volatile("s_waitcnt lgkmcnt(0)" ::: "memory")
; #define DEEP_LOAD(I, v, idx) do { if ((idx) < hi) { moe_item(wg, wu, wd, wsb, (idx), I); xf8_load(I.W, I.N, I.k0, I.n0, lane, v); } } while (0)
; #define DEEP_STEP(I, v, idx) do { if ((idx) < hi) { xf8_proc(v, I.K, I.WT, I.drow0, I.k0, I.scale, scr, lane); DEEP_LOAD(I, v, (idx) + 4 * stride); } } while (0)
; __device__ __forceinline__ void xf8_proc(const f32x4 (&v)[8], int K, unsigned char* WT, int drow0, int k0, float scale, LAS float* scr, int lane) {
; #pragma unroll
;     for (int i = 0; i < 8; ++i) { LAS float* d_ = scr + (8 * i + (lane >> 3)) * 33 + 4 * (lane & 7); d_[0] = v[i].x; d_[1] = v[i].y; d_[2] = v[i].z; d_[3] = v[i].w; }
;     LDS_WAIT(); asm volatile("" ::: "memory");
;     const int c = lane & 7;
; #pragma unroll
;     for (int j = 0; j < 4; ++j) { const int n = (lane >> 3) + 8 * j; const LAS float* s = scr + (8 * c) * 33 + n;
;         pg8::u32x2 o; o.x = pg8::pk4_fp8(s[0 * 33] * scale, s[1 * 33] * scale, s[2 * 33] * scale, s[3 * 33] * scale); o.y = pg8::pk4_fp8(s[4 * 33] * scale, s[5 * 33] * scale, s[6 * 33] * scale, s[7 * 33] * scale);
;         __builtin_nontemporal_store(o, (GAS pg8::u32x2*)(WT + (size_t)(drow0 + n) * K + k0 + 8 * c)); }
;     LDS_WAIT(); asm volatile("" ::: "memory");
; }
; __device__ __forceinline__ void moe_deep_items(const float* wg, const float* wu, const float* wd, unsigned char* wsb, int lo, int hi, int first, int stride, LAS float* scr, int lane) {
;     ...
;     DEEP_LOAD(I0, v0, it); DEEP_LOAD(I1, v1, it + stride); DEEP_LOAD(I2, v2, it + 2 * stride); DEEP_LOAD(I3, v3, it + 3 * stride);
;     for (; it < hi; it += 4 * stride) { DEEP_STEP(I0, v0, it); DEEP_STEP(I1, v1, it + stride); DEEP_STEP(I2, v2, it + 2 * stride); DEEP_STEP(I3, v3, it + 3 * stride); }
.LBB0_850:
	s_cmpk_gt_i32 s73, 0xbff
	s_cbranch_scc1 .LBB0_858
	ds_write2_b32 v140, v34, v35 offset1:1
	ds_write2_b32 v140, v36, v37 offset0:2 offset1:3
	ds_write2_b32 v141, v38, v39 offset1:1
	ds_write2_b32 v142, v40, v41 offset1:1
	ds_write2_b32 v143, v42, v43 offset1:1
	ds_write2_b32 v144, v44, v45 offset1:1
	ds_write2_b32 v145, v46, v47 offset1:1
	ds_write2_b32 v146, v48, v49 offset1:1
	ds_write2_b32 v147, v50, v51 offset1:1
	ds_write2_b32 v148, v52, v53 offset1:1
	ds_write2_b32 v149, v54, v55 offset1:1
	ds_write2_b32 v150, v56, v57 offset1:1
	ds_write2_b32 v151, v58, v59 offset1:1
	ds_write2_b32 v152, v60, v61 offset1:1
	ds_write2_b32 v153, v62, v63 offset1:1
	ds_write2_b32 v154, v64, v65 offset1:1
	s_waitcnt lgkmcnt(0)
	ds_read2_b32 v[156:157], v139 offset1:8
	ds_read2_b32 v[158:159], v139 offset0:33 offset1:41
	ds_read2_b32 v[160:161], v139 offset0:66 offset1:74
	ds_read2_b32 v[168:169], v139 offset0:99 offset1:107
	ds_read2_b32 v[170:171], v139 offset0:132 offset1:140
	ds_read2_b32 v[172:173], v139 offset0:165 offset1:173
	v_mov_b32_e32 v174, v135
	s_waitcnt lgkmcnt(5)
	v_mul_f32_e32 v134, s42, v156
	s_waitcnt lgkmcnt(4)
	v_mul_f32_e32 v155, s42, v158
	ds_read2_b32 v[176:177], v139 offset0:198 offset1:206
	ds_read2_b32 v[178:179], v139 offset0:231 offset1:239
	v_cvt_pk_fp8_f32 v174, v134, v155
	s_waitcnt lgkmcnt(3)
	v_mul_f32_e32 v134, s42, v170
	s_waitcnt lgkmcnt(2)
	v_mul_f32_e32 v155, s42, v172
	v_mov_b32_e32 v175, v135
	v_cvt_pk_fp8_f32 v175, v134, v155
	s_ashr_i32 s0, s41, 31
	s_add_u32 s4, s12, s41
	s_addc_u32 s5, s13, s0
	s_waitcnt lgkmcnt(1)
	v_mul_f32_e32 v134, s42, v176
	s_waitcnt lgkmcnt(0)
	v_mul_f32_e32 v155, s42, v178
	v_lshl_add_u64 v[166:167], s[4:5], 0, v[132:133]
	v_mul_f32_e32 v156, s42, v160
	v_mul_f32_e32 v158, s42, v168
	v_cvt_pk_fp8_f32 v175, v134, v155 op_sel:[0,0,1]
	v_add_u32_e32 v134, s40, v131
	v_cvt_pk_fp8_f32 v174, v156, v158 op_sel:[0,0,1]
	v_mad_i64_i32 v[180:181], s[4:5], v134, s43, v[166:167]
	v_mul_f32_e32 v134, s42, v157
	v_mul_f32_e32 v155, s42, v159
	v_mov_b32_e32 v156, v135
	v_cvt_pk_fp8_f32 v156, v134, v155
	v_mul_f32_e32 v134, s42, v171
	v_mul_f32_e32 v155, s42, v173
	v_mov_b32_e32 v157, v135
	v_cvt_pk_fp8_f32 v157, v134, v155
	v_mul_f32_e32 v158, s42, v161
	v_mul_f32_e32 v159, s42, v169
	v_mul_f32_e32 v134, s42, v177
	v_mul_f32_e32 v155, s42, v179
	v_cvt_pk_fp8_f32 v156, v158, v159 op_sel:[0,0,1]
	v_cvt_pk_fp8_f32 v157, v134, v155 op_sel:[0,0,1]
	v_add_u32_e32 v134, s40, v136
	global_store_dwordx2 v[180:181], v[174:175], off nt
	v_mad_i64_i32 v[160:161], s[4:5], v134, s43, v[166:167]
	ds_read2_b32 v[158:159], v139 offset0:16 offset1:24
	ds_read2_b32 v[168:169], v139 offset0:49 offset1:57
	ds_read2_b32 v[170:171], v139 offset0:82 offset1:90
	global_store_dwordx2 v[160:161], v[156:157], off nt
	ds_read2_b32 v[156:157], v139 offset0:115 offset1:123
	ds_read2_b32 v[160:161], v139 offset0:148 offset1:156
	ds_read2_b32 v[172:173], v139 offset0:181 offset1:189
	s_waitcnt lgkmcnt(5)
	v_mul_f32_e32 v134, s42, v158
	s_waitcnt lgkmcnt(4)
	v_mul_f32_e32 v155, s42, v168
	v_mov_b32_e32 v174, v135
	ds_read2_b32 v[176:177], v139 offset0:214 offset1:222
	ds_read2_b32 v[178:179], v139 offset0:247 offset1:255
	v_cvt_pk_fp8_f32 v174, v134, v155
	s_waitcnt lgkmcnt(3)
	v_mul_f32_e32 v134, s42, v160
	s_waitcnt lgkmcnt(2)
	v_mul_f32_e32 v155, s42, v172
	v_mov_b32_e32 v175, v135
	v_cvt_pk_fp8_f32 v175, v134, v155
	s_waitcnt lgkmcnt(1)
	v_mul_f32_e32 v134, s42, v176
	s_waitcnt lgkmcnt(0)
	v_mul_f32_e32 v155, s42, v178
	v_mul_f32_e32 v158, s42, v170
	v_mul_f32_e32 v156, s42, v156
	v_cvt_pk_fp8_f32 v175, v134, v155 op_sel:[0,0,1]
	v_add_u32_e32 v134, s40, v137
	v_cvt_pk_fp8_f32 v174, v158, v156 op_sel:[0,0,1]
	v_mad_i64_i32 v[180:181], s[4:5], v134, s43, v[166:167]
	v_mul_f32_e32 v134, s42, v159
	v_mul_f32_e32 v155, s42, v169
	v_mov_b32_e32 v156, v135
	v_mul_f32_e32 v159, s42, v157
	v_cvt_pk_fp8_f32 v156, v134, v155
	v_mul_f32_e32 v134, s42, v161
	v_mul_f32_e32 v155, s42, v173
	v_mov_b32_e32 v157, v135
	v_cvt_pk_fp8_f32 v157, v134, v155
	v_mul_f32_e32 v158, s42, v171
	v_mul_f32_e32 v134, s42, v177
	v_mul_f32_e32 v155, s42, v179
	v_cvt_pk_fp8_f32 v156, v158, v159 op_sel:[0,0,1]
	v_cvt_pk_fp8_f32 v157, v134, v155 op_sel:[0,0,1]
	v_add_u32_e32 v134, s40, v138
	v_mad_i64_i32 v[158:159], s[4:5], v134, s43, v[166:167]
	global_store_dwordx2 v[180:181], v[174:175], off nt
	global_store_dwordx2 v[158:159], v[156:157], off nt
	s_waitcnt lgkmcnt(0)
	s_cmpk_gt_i32 s73, -1025
	s_cbranch_scc1 .LBB0_858
	s_add_i32 s0, s70, 0xfffff800
	s_mul_hi_i32 s1, s0, 0x92492493
	s_add_i32 s1, s1, s0
	s_mul_hi_i32 s0, s0, 0x30c30c31
	s_lshr_b32 s3, s1, 31
	s_ashr_i32 s5, s1, 10
	s_lshr_b32 s1, s0, 31
	s_ashr_i32 s4, s0, 10
	s_add_i32 s4, s4, s1
	s_add_i32 s5, s5, s3
	s_mul_i32 s3, s4, -3
	s_add_i32 s3, s3, s5
	s_mov_b64 s[22:23], -1
	s_cmp_gt_i32 s3, 1
	s_mul_hi_i32 s6, s4, 0xe00000
	s_mul_i32 s7, s4, 0xe00000
	s_cbranch_scc0 .LBB0_854
	s_and_b32 s40, s72, 0x3e0
	s_add_u32 s18, s60, s7
	s_addc_u32 s19, s61, s6
	s_mul_i32 s1, s4, 0x380000
	s_mul_hi_i32 s0, s4, 0x380000
	s_add_u32 s12, s30, s1
	s_addc_u32 s13, s31, s0
	s_mul_i32 s0, s5, 0xfffff200
	s_add_i32 s0, s71, s0
	s_addk_i32 s0, 0x2000
	s_and_b32 s41, s0, 0xffffffc0
	s_mov_b64 s[22:23], 0

; __device__ __forceinline__ unsigned pk4_fp8(float a, float b, float c, float d) { int w = 0; w = __builtin_amdgcn_cvt_pk_fp8_f32(a, b, w, false); w = __builtin_amdgcn_cvt_pk_fp8_f32(c, d, w, true); return (unsigned)w; }
; #define GAS __attribute__((address_space(1)))
; #define LAS __attribute__((address_space(3)))
; #define LDS_WAIT() asm volatile("s_waitcnt lgkmcnt(0)" ::: "memory")
; #define DEEP_LOAD(I, v, idx) do { if ((idx) < hi) { moe_item(wg, wu, wd, wsb, (idx), I); xf8_load(I.W, I.N, I.k0, I.n0, lane, v); } } while (0)
; #define DEEP_STEP(I, v, idx) do { if ((idx) < hi) { xf8_proc(v, I.K, I.WT, I.drow0, I.k0, I.scale, scr, lane); DEEP_LOAD(I, v, (idx) + 4 * stride); } } while (0)
; __device__ __forceinline__ void xf8_proc(const f32x4 (&v)[8], int K, unsigned char* WT, int drow0, int k0, float scale, LAS float* scr, int lane) {
; #pragma unroll
;     for (int i = 0; i < 8; ++i) { LAS float* d_ = scr + (8 * i + (lane >> 3)) * 33 + 4 * (lane & 7); d_[0] = v[i].x; d_[1] = v[i].y; d_[2] = v[i].z; d_[3] = v[i].w; }
;     LDS_WAIT(); asm volatile("" ::: "memory");
;     const int c = lane & 7;
; #pragma unroll
;     for (int j = 0; j < 4; ++j) { const int n = (lane >> 3) + 8 * j; const LAS float* s = scr + (8 * c) * 33 + n;
;         pg8::u32x2 o; o.x = pg8::pk4_fp8(s[0 * 33] * scale, s[1 * 33] * scale, s[2 * 33] * scale, s[3 * 33] * scale); o.y = pg8::pk4_fp8(s[4 * 33] * scale, s[5 * 33] * scale, s[6 * 33] * scale, s[7 * 33] * scale);
;         __builtin_nontemporal_store(o, (GAS pg8::u32x2*)(WT + (size_t)(drow0 + n) * K + k0 + 8 * c)); }
;     LDS_WAIT(); asm volatile("" ::: "memory");
; }
; __device__ __forceinline__ void moe_deep_items(const float* wg, const float* wu, const float* wd, unsigned char* wsb, int lo, int hi, int first, int stride, LAS float* scr, int lane) {
;     ...
;     DEEP_LOAD(I0, v0, it); DEEP_LOAD(I1, v1, it + stride); DEEP_LOAD(I2, v2, it + 2 * stride); DEEP_LOAD(I3, v3, it + 3 * stride);
;     for (; it < hi; it += 4 * stride) { DEEP_STEP(I0, v0, it); DEEP_STEP(I1, v1, it + stride); DEEP_STEP(I2, v2, it + 2 * stride); DEEP_STEP(I3, v3, it + 3 * stride); }
.LBB0_858:
	s_cmpk_gt_i32 s73, 0x7ff
	s_cbranch_scc1 .LBB0_860
	ds_write2_b32 v140, v66, v67 offset1:1
	ds_write2_b32 v140, v68, v69 offset0:2 offset1:3
	ds_write2_b32 v141, v70, v71 offset1:1
	ds_write2_b32 v142, v72, v73 offset1:1
	ds_write2_b32 v143, v74, v75 offset1:1
	ds_write2_b32 v144, v76, v77 offset1:1
	ds_write2_b32 v145, v78, v79 offset1:1
	ds_write2_b32 v146, v80, v81 offset1:1
	ds_write2_b32 v147, v82, v83 offset1:1
	ds_write2_b32 v148, v84, v85 offset1:1
	ds_write2_b32 v149, v86, v87 offset1:1
	ds_write2_b32 v150, v88, v89 offset1:1
	ds_write2_b32 v151, v90, v91 offset1:1
	ds_write2_b32 v152, v92, v93 offset1:1
	ds_write2_b32 v153, v94, v95 offset1:1
	ds_write2_b32 v154, v96, v97 offset1:1
	s_waitcnt lgkmcnt(0)
	ds_read2_b32 v[156:157], v139 offset1:8
	ds_read2_b32 v[158:159], v139 offset0:33 offset1:41
	ds_read2_b32 v[160:161], v139 offset0:66 offset1:74
	ds_read2_b32 v[168:169], v139 offset0:99 offset1:107
	ds_read2_b32 v[170:171], v139 offset0:132 offset1:140
	ds_read2_b32 v[172:173], v139 offset0:165 offset1:173
	v_mov_b32_e32 v174, v135
	s_waitcnt lgkmcnt(5)
	v_mul_f32_e32 v134, s46, v156
	s_waitcnt lgkmcnt(4)
	v_mul_f32_e32 v155, s46, v158
	ds_read2_b32 v[176:177], v139 offset0:198 offset1:206
	ds_read2_b32 v[178:179], v139 offset0:231 offset1:239
	v_cvt_pk_fp8_f32 v174, v134, v155
	s_waitcnt lgkmcnt(3)
	v_mul_f32_e32 v134, s46, v170
	s_waitcnt lgkmcnt(2)
	v_mul_f32_e32 v155, s46, v172
	v_mov_b32_e32 v175, v135
	v_cvt_pk_fp8_f32 v175, v134, v155
	s_ashr_i32 s0, s45, 31
	s_add_u32 s4, s14, s45
	s_addc_u32 s5, s15, s0
	s_waitcnt lgkmcnt(1)
	v_mul_f32_e32 v134, s46, v176
	s_waitcnt lgkmcnt(0)
	v_mul_f32_e32 v155, s46, v178
	v_lshl_add_u64 v[166:167], s[4:5], 0, v[132:133]
	v_mul_f32_e32 v156, s46, v160
	v_mul_f32_e32 v158, s46, v168
	v_cvt_pk_fp8_f32 v175, v134, v155 op_sel:[0,0,1]
	v_add_u32_e32 v134, s44, v131
	v_cvt_pk_fp8_f32 v174, v156, v158 op_sel:[0,0,1]
	v_mad_i64_i32 v[180:181], s[4:5], v134, s47, v[166:167]
	v_mul_f32_e32 v134, s46, v157
	v_mul_f32_e32 v155, s46, v159
	v_mov_b32_e32 v156, v135
	v_cvt_pk_fp8_f32 v156, v134, v155
	v_mul_f32_e32 v134, s46, v171
	v_mul_f32_e32 v155, s46, v173
	v_mov_b32_e32 v157, v135
	v_cvt_pk_fp8_f32 v157, v134, v155
	v_mul_f32_e32 v158, s46, v161
	v_mul_f32_e32 v159, s46, v169
	v_mul_f32_e32 v134, s46, v177
	v_mul_f32_e32 v155, s46, v179
	v_cvt_pk_fp8_f32 v156, v158, v159 op_sel:[0,0,1]
	v_cvt_pk_fp8_f32 v157, v134, v155 op_sel:[0,0,1]
	v_add_u32_e32 v134, s44, v136
	global_store_dwordx2 v[180:181], v[174:175], off nt
	v_mad_i64_i32 v[160:161], s[4:5], v134, s47, v[166:167]
	ds_read2_b32 v[158:159], v139 offset0:16 offset1:24
	ds_read2_b32 v[168:169], v139 offset0:49 offset1:57
	ds_read2_b32 v[170:171], v139 offset0:82 offset1:90
	global_store_dwordx2 v[160:161], v[156:157], off nt
	ds_read2_b32 v[156:157], v139 offset0:115 offset1:123
	ds_read2_b32 v[160:161], v139 offset0:148 offset1:156
	ds_read2_b32 v[172:173], v139 offset0:181 offset1:189
	s_waitcnt lgkmcnt(5)
	v_mul_f32_e32 v134, s46, v158
	s_waitcnt lgkmcnt(4)
	v_mul_f32_e32 v155, s46, v168
	v_mov_b32_e32 v174, v135
	ds_read2_b32 v[176:177], v139 offset0:214 offset1:222
	ds_read2_b32 v[178:179], v139 offset0:247 offset1:255
	v_cvt_pk_fp8_f32 v174, v134, v155
	s_waitcnt lgkmcnt(3)
	v_mul_f32_e32 v134, s46, v160
	s_waitcnt lgkmcnt(2)
	v_mul_f32_e32 v155, s46, v172
	v_mov_b32_e32 v175, v135
	v_cvt_pk_fp8_f32 v175, v134, v155
	s_waitcnt lgkmcnt(1)
	v_mul_f32_e32 v134, s46, v176
	s_waitcnt lgkmcnt(0)
	v_mul_f32_e32 v155, s46, v178
	v_mul_f32_e32 v158, s46, v170
	v_mul_f32_e32 v156, s46, v156
	v_cvt_pk_fp8_f32 v175, v134, v155 op_sel:[0,0,1]
	v_add_u32_e32 v134, s44, v137
	v_cvt_pk_fp8_f32 v174, v158, v156 op_sel:[0,0,1]
	v_mad_i64_i32 v[180:181], s[4:5], v134, s47, v[166:167]
	v_mul_f32_e32 v134, s46, v159
	v_mul_f32_e32 v155, s46, v169
	v_mov_b32_e32 v156, v135
	v_mul_f32_e32 v159, s46, v157
	v_cvt_pk_fp8_f32 v156, v134, v155
	v_mul_f32_e32 v134, s46, v161
	v_mul_f32_e32 v155, s46, v173
	v_mov_b32_e32 v157, v135
	v_cvt_pk_fp8_f32 v157, v134, v155
	v_mul_f32_e32 v158, s46, v171
	v_mul_f32_e32 v134, s46, v177
	v_mul_f32_e32 v155, s46, v179
	v_cvt_pk_fp8_f32 v156, v158, v159 op_sel:[0,0,1]
	v_cvt_pk_fp8_f32 v157, v134, v155 op_sel:[0,0,1]
	v_add_u32_e32 v134, s44, v138
	v_mad_i64_i32 v[158:159], s[4:5], v134, s47, v[166:167]
	global_store_dwordx2 v[180:181], v[174:175], off nt
	global_store_dwordx2 v[158:159], v[156:157], off nt
	s_waitcnt lgkmcnt(0)
	s_cmpk_gt_i32 s73, -2049
	s_cbranch_scc0 .LBB0_866
.LBB0_860:
	s_cmpk_gt_i32 s73, 0x3ff
	s_cbranch_scc1 .LBB0_842
; __device__ __forceinline__ unsigned pk4_fp8(float a, float b, float c, float d) { int w = 0; w = __builtin_amdgcn_cvt_pk_fp8_f32(a, b, w, false); w = __builtin_amdgcn_cvt_pk_fp8_f32(c, d, w, true); return (unsigned)w; }
; #define GAS __attribute__((address_space(1)))
; #define LAS __attribute__((address_space(3)))
; #define LDS_WAIT() asm volatile("s_waitcnt lgkmcnt(0)" ::: "memory")
; #define DEEP_LOAD(I, v, idx) do { if ((idx) < hi) { moe_item(wg, wu, wd, wsb, (idx), I); xf8_load(I.W, I.N, I.k0, I.n0, lane, v); } } while (0)
; #define DEEP_STEP(I, v, idx) do { if ((idx) < hi) { xf8_proc(v, I.K, I.WT, I.drow0, I.k0, I.scale, scr, lane); DEEP_LOAD(I, v, (idx) + 4 * stride); } } while (0)
; __device__ __forceinline__ void xf8_proc(const f32x4 (&v)[8], int K, unsigned char* WT, int drow0, int k0, float scale, LAS float* scr, int lane) {
; #pragma unroll
;     for (int i = 0; i < 8; ++i) { LAS float* d_ = scr + (8 * i + (lane >> 3)) * 33 + 4 * (lane & 7); d_[0] = v[i].x; d_[1] = v[i].y; d_[2] = v[i].z; d_[3] = v[i].w; }
;     LDS_WAIT(); asm volatile("" ::: "memory");
;     const int c = lane & 7;
; #pragma unroll
;     for (int j = 0; j < 4; ++j) { const int n = (lane >> 3) + 8 * j; const LAS float* s = scr + (8 * c) * 33 + n;
;         pg8::u32x2 o; o.x = pg8::pk4_fp8(s[0 * 33] * scale, s[1 * 33] * scale, s[2 * 33] * scale, s[3 * 33] * scale); o.y = pg8::pk4_fp8(s[4 * 33] * scale, s[5 * 33] * scale, s[6 * 33] * scale, s[7 * 33] * scale);
;         __builtin_nontemporal_store(o, (GAS pg8::u32x2*)(WT + (size_t)(drow0 + n) * K + k0 + 8 * c)); }
;     LDS_WAIT(); asm volatile("" ::: "memory");
; }
; __device__ __forceinline__ void moe_deep_items(const float* wg, const float* wu, const float* wd, unsigned char* wsb, int lo, int hi, int first, int stride, LAS float* scr, int lane) {
;     ...
;     DEEP_LOAD(I0, v0, it); DEEP_LOAD(I1, v1, it + stride); DEEP_LOAD(I2, v2, it + 2 * stride); DEEP_LOAD(I3, v3, it + 3 * stride);
;     for (; it < hi; it += 4 * stride) { DEEP_STEP(I0, v0, it); DEEP_STEP(I1, v1, it + stride); DEEP_STEP(I2, v2, it + 2 * stride); DEEP_STEP(I3, v3, it + 3 * stride); }
.LBB0_861:
	ds_write2_b32 v140, v98, v99 offset1:1
	ds_write2_b32 v140, v100, v101 offset0:2 offset1:3
	ds_write2_b32 v141, v102, v103 offset1:1
	ds_write2_b32 v142, v104, v105 offset1:1
	ds_write2_b32 v143, v106, v107 offset1:1
	ds_write2_b32 v144, v108, v109 offset1:1
	ds_write2_b32 v145, v110, v111 offset1:1
	ds_write2_b32 v146, v112, v113 offset1:1
	ds_write2_b32 v147, v114, v115 offset1:1
	ds_write2_b32 v148, v116, v117 offset1:1
	ds_write2_b32 v149, v118, v119 offset1:1
	ds_write2_b32 v150, v120, v121 offset1:1
	ds_write2_b32 v151, v122, v123 offset1:1
	ds_write2_b32 v152, v124, v125 offset1:1
	ds_write2_b32 v153, v126, v127 offset1:1
	ds_write2_b32 v154, v128, v129 offset1:1
	s_waitcnt lgkmcnt(0)
	ds_read2_b32 v[156:157], v139 offset1:8
	ds_read2_b32 v[158:159], v139 offset0:33 offset1:41
	ds_read2_b32 v[160:161], v139 offset0:66 offset1:74
	ds_read2_b32 v[168:169], v139 offset0:99 offset1:107
	ds_read2_b32 v[170:171], v139 offset0:132 offset1:140
	ds_read2_b32 v[172:173], v139 offset0:165 offset1:173
	v_mov_b32_e32 v174, v135
	s_waitcnt lgkmcnt(5)
	v_mul_f32_e32 v134, s50, v156
	s_waitcnt lgkmcnt(4)
	v_mul_f32_e32 v155, s50, v158
	ds_read2_b32 v[176:177], v139 offset0:198 offset1:206
	ds_read2_b32 v[178:179], v139 offset0:231 offset1:239
	v_cvt_pk_fp8_f32 v174, v134, v155
	s_waitcnt lgkmcnt(3)
	v_mul_f32_e32 v134, s50, v170
	s_waitcnt lgkmcnt(2)
	v_mul_f32_e32 v155, s50, v172
	v_mov_b32_e32 v175, v135
	v_cvt_pk_fp8_f32 v175, v134, v155
	s_ashr_i32 s0, s49, 31
	s_add_u32 s4, s16, s49
	s_addc_u32 s5, s17, s0
	s_waitcnt lgkmcnt(1)
	v_mul_f32_e32 v134, s50, v176
	s_waitcnt lgkmcnt(0)
	v_mul_f32_e32 v155, s50, v178
	v_lshl_add_u64 v[166:167], s[4:5], 0, v[132:133]
	v_mul_f32_e32 v156, s50, v160
	v_mul_f32_e32 v158, s50, v168
	v_cvt_pk_fp8_f32 v175, v134, v155 op_sel:[0,0,1]
	v_add_u32_e32 v134, s48, v131
	v_cvt_pk_fp8_f32 v174, v156, v158 op_sel:[0,0,1]
	v_mad_i64_i32 v[180:181], s[4:5], v134, s51, v[166:167]
	v_mul_f32_e32 v134, s50, v157
	v_mul_f32_e32 v155, s50, v159
	v_mov_b32_e32 v156, v135
	v_cvt_pk_fp8_f32 v156, v134, v155
	v_mul_f32_e32 v134, s50, v171
	v_mul_f32_e32 v155, s50, v173
	v_mov_b32_e32 v157, v135
	v_cvt_pk_fp8_f32 v157, v134, v155
	v_mul_f32_e32 v158, s50, v161
	v_mul_f32_e32 v159, s50, v169
	v_mul_f32_e32 v134, s50, v177
	v_mul_f32_e32 v155, s50, v179
	v_cvt_pk_fp8_f32 v156, v158, v159 op_sel:[0,0,1]
	v_cvt_pk_fp8_f32 v157, v134, v155 op_sel:[0,0,1]
	v_add_u32_e32 v134, s48, v136
	global_store_dwordx2 v[180:181], v[174:175], off nt
	v_mad_i64_i32 v[160:161], s[4:5], v134, s51, v[166:167]
	ds_read2_b32 v[158:159], v139 offset0:16 offset1:24
	ds_read2_b32 v[168:169], v139 offset0:49 offset1:57
	ds_read2_b32 v[170:171], v139 offset0:82 offset1:90
	global_store_dwordx2 v[160:161], v[156:157], off nt
	ds_read2_b32 v[156:157], v139 offset0:115 offset1:123
	ds_read2_b32 v[160:161], v139 offset0:148 offset1:156
	ds_read2_b32 v[172:173], v139 offset0:181 offset1:189
	s_waitcnt lgkmcnt(5)
	v_mul_f32_e32 v134, s50, v158
	s_waitcnt lgkmcnt(4)
	v_mul_f32_e32 v155, s50, v168
	v_mov_b32_e32 v174, v135
	ds_read2_b32 v[176:177], v139 offset0:214 offset1:222
	ds_read2_b32 v[178:179], v139 offset0:247 offset1:255
	v_cvt_pk_fp8_f32 v174, v134, v155
	s_waitcnt lgkmcnt(3)
	v_mul_f32_e32 v134, s50, v160
	s_waitcnt lgkmcnt(2)
	v_mul_f32_e32 v155, s50, v172
	v_mov_b32_e32 v175, v135
	v_cvt_pk_fp8_f32 v175, v134, v155
	s_waitcnt lgkmcnt(1)
	v_mul_f32_e32 v134, s50, v176
	s_waitcnt lgkmcnt(0)
	v_mul_f32_e32 v155, s50, v178
	v_mul_f32_e32 v158, s50, v170
	v_mul_f32_e32 v156, s50, v156
	v_cvt_pk_fp8_f32 v175, v134, v155 op_sel:[0,0,1]
	v_add_u32_e32 v134, s48, v137
	v_cvt_pk_fp8_f32 v174, v158, v156 op_sel:[0,0,1]
	v_mad_i64_i32 v[180:181], s[4:5], v134, s51, v[166:167]
	v_mul_f32_e32 v134, s50, v159
	v_mul_f32_e32 v155, s50, v169
	v_mov_b32_e32 v156, v135
	v_mul_f32_e32 v159, s50, v157
	v_cvt_pk_fp8_f32 v156, v134, v155
	v_mul_f32_e32 v134, s50, v161
	v_mul_f32_e32 v155, s50, v173
	v_mov_b32_e32 v157, v135
	v_cvt_pk_fp8_f32 v157, v134, v155
	v_mul_f32_e32 v158, s50, v171
	v_mul_f32_e32 v134, s50, v177
	v_mul_f32_e32 v155, s50, v179
	v_cvt_pk_fp8_f32 v156, v158, v159 op_sel:[0,0,1]
	v_cvt_pk_fp8_f32 v157, v134, v155 op_sel:[0,0,1]
	v_add_u32_e32 v134, s48, v138
	v_mad_i64_i32 v[158:159], s[4:5], v134, s51, v[166:167]
	global_store_dwordx2 v[180:181], v[174:175], off nt
	global_store_dwordx2 v[158:159], v[156:157], off nt
	s_waitcnt lgkmcnt(0)
	s_cmpk_gt_i32 s73, -3073
	s_cbranch_scc1 .LBB0_842
	s_mul_hi_i32 s0, s70, 0x92492493
	s_add_i32 s0, s0, s70
	s_lshr_b32 s1, s0, 31
	s_ashr_i32 s5, s0, 10
	s_mul_hi_i32 s0, s70, 0x30c30c31
	s_add_i32 s5, s5, s1
	s_lshr_b32 s1, s0, 31
	s_ashr_i32 s4, s0, 10
	s_add_i32 s4, s4, s1
	s_mul_i32 s3, s4, -3
	s_add_i32 s3, s3, s5
	s_mov_b64 s[22:23], -1
	s_cmp_gt_i32 s3, 1
	s_mul_hi_i32 s6, s4, 0xe00000
	s_mul_i32 s7, s4, 0xe00000
	s_cbranch_scc0 .LBB0_864
	s_and_b32 s48, s72, 0x3e0
	s_add_u32 s18, s60, s7
	s_addc_u32 s19, s61, s6
	s_mul_i32 s1, s4, 0x380000
	s_mul_hi_i32 s0, s4, 0x380000
	s_add_u32 s16, s30, s1
	s_addc_u32 s17, s31, s0
	s_mul_i32 s0, s5, 0xfffff200
	s_add_i32 s0, s71, s0
	s_addk_i32 s0, 0x3000
	s_and_b32 s49, s0, 0xffffffc0
	s_mov_b64 s[22:23], 0

; #define GAS __attribute__((address_space(1)))
; #define DEEP_LOAD(I, v, idx) do { if ((idx) < hi) { moe_item(wg, wu, wd, wsb, (idx), I); xf8_load(I.W, I.N, I.k0, I.n0, lane, v); } } while (0)
; #define DEEP_STEP(I, v, idx) do { if ((idx) < hi) { xf8_proc(v, I.K, I.WT, I.drow0, I.k0, I.scale, scr, lane); DEEP_LOAD(I, v, (idx) + 4 * stride); } } while (0)
; __device__ __forceinline__ void xf8_load(const float* W, int N, int k0, int n0, int lane, f32x4 (&v)[8]) {
; #pragma unroll
;     for (int i = 0; i < 8; ++i) v[i] = __builtin_nontemporal_load((const GAS f32x4*)(W + (size_t)(k0 + 8 * i + (lane >> 3)) * N + n0 + 4 * (lane & 7)));
; }
; __device__ __forceinline__ void moe_deep_items(const float* wg, const float* wu, const float* wd, unsigned char* wsb, int lo, int hi, int first, int stride, LAS float* scr, int lane) {
;     ...
;     DEEP_LOAD(I0, v0, it); DEEP_LOAD(I1, v1, it + stride); DEEP_LOAD(I2, v2, it + 2 * stride); DEEP_LOAD(I3, v3, it + 3 * stride);
;     for (; it < hi; it += 4 * stride) { DEEP_STEP(I0, v0, it); DEEP_STEP(I1, v1, it + stride); DEEP_STEP(I2, v2, it + 2 * stride); DEEP_STEP(I3, v3, it + 3 * stride); }
.LBB0_871:
	s_ashr_i32 s25, s24, 31
	s_lshl_b64 s[4:5], s[24:25], 2
	s_add_u32 s4, s18, s4
	v_or_b32_e32 v94, s45, v131
	s_addc_u32 s5, s19, s5
	v_lshlrev_b32_e32 v134, 2, v130
	v_lshl_add_u64 v[90:91], s[4:5], 0, v[134:135]
	v_mad_i64_i32 v[66:67], s[4:5], s22, v94, 0
	v_or_b32_e32 v68, 8, v94
	v_or_b32_e32 v74, 16, v94
	v_or_b32_e32 v76, 24, v94
	v_or_b32_e32 v82, 32, v94
	v_or_b32_e32 v84, 40, v94
	v_or_b32_e32 v92, 48, v94
	v_or_b32_e32 v94, 56, v94
	v_mad_i64_i32 v[68:69], s[4:5], s22, v68, 0
	v_mad_i64_i32 v[74:75], s[4:5], s22, v74, 0
	v_mad_i64_i32 v[76:77], s[4:5], s22, v76, 0
	v_mad_i64_i32 v[82:83], s[4:5], s22, v82, 0
	v_mad_i64_i32 v[84:85], s[4:5], s22, v84, 0
	v_mad_i64_i32 v[92:93], s[4:5], s22, v92, 0
	v_mad_i64_i32 v[94:95], s[4:5], s22, v94, 0
	v_lshl_add_u64 v[66:67], v[66:67], 2, v[90:91]
	v_lshl_add_u64 v[70:71], v[68:69], 2, v[90:91]
	v_lshl_add_u64 v[74:75], v[74:75], 2, v[90:91]
	v_lshl_add_u64 v[78:79], v[76:77], 2, v[90:91]
	v_lshl_add_u64 v[82:83], v[82:83], 2, v[90:91]
	v_lshl_add_u64 v[86:87], v[84:85], 2, v[90:91]
	v_lshl_add_u64 v[92:93], v[92:93], 2, v[90:91]
	v_lshl_add_u64 v[94:95], v[94:95], 2, v[90:91]
	global_load_dwordx4 v[66:69], v[66:67], off nt
	s_nop 0
	global_load_dwordx4 v[70:73], v[70:71], off nt
	s_nop 0
	global_load_dwordx4 v[74:77], v[74:75], off nt
	s_nop 0
	global_load_dwordx4 v[78:81], v[78:79], off nt
	s_nop 0
	global_load_dwordx4 v[82:85], v[82:83], off nt
	s_nop 0
	global_load_dwordx4 v[86:89], v[86:87], off nt
	s_nop 0
	global_load_dwordx4 v[90:93], v[92:93], off nt
	s_nop 0
	global_load_dwordx4 v[94:97], v[94:95], off nt
	s_cmpk_gt_i32 s73, 0x3ff
	s_cbranch_scc1 .LBB0_842
	s_branch .LBB0_861
